# combined: rope epilogue quads paired (layer-1 q/k), ssd_out next-head operand prefetch, post0 lane-pair exchanges as DPP moves
# speedup vs baseline: 1.0054x; 1.0048x over previous
.LBB0_561:
	s_andn2_saveexec_b64 s[2:3], s[2:3]
	v_mul_f32_e64 v71, |v1|, s65
	v_rndne_f32_e32 v73, v71
	v_cvt_i32_f32_e32 v72, v73
	v_fma_f32 v71, v73, s66, |v1|
	v_fmac_f32_e32 v71, 0xb3a22168, v73
	v_fmac_f32_e32 v71, 0xa7c234c4, v73
	s_or_b64 exec, exec, s[2:3]
	v_mul_f32_e32 v73, v71, v71
	v_mov_b32_e32 v74, 0x3c0881c4
	v_fmamk_f32 v74, v73, 0xb94c1982, v74
	v_fmaak_f32 v74, v73, v74, 0xbe2aaa9d
	v_mul_f32_e32 v74, v73, v74
	v_fmac_f32_e32 v71, v71, v74
	v_mov_b32_e32 v74, 0xbab64f3b
	v_fmamk_f32 v74, v73, 0x37d75334, v74
	v_fmaak_f32 v74, v73, v74, 0x3d2aabf7
	v_fmaak_f32 v74, v73, v74, 0xbf000004
	global_load_dwordx4 v[78:81], v[102:103], off offset:16
	global_load_dwordx4 v[90:93], v[102:103], off
	v_fma_f32 v73, v73, v74, 1.0
	v_lshlrev_b32_e32 v74, 30, v72
	v_and_b32_e32 v72, 1, v72
	v_cmp_eq_u32_e32 vcc, 0, v72
	v_xor_b32_e32 v70, v70, v1
	v_and_b32_e32 v75, 0x80000000, v74
	v_cndmask_b32_e32 v72, v73, v71, vcc
	v_xor_b32_e32 v71, 0x80000000, v71
	v_xor_b32_e32 v70, v70, v72
	v_cndmask_b32_e32 v71, v71, v73, vcc
	v_xor_b32_e32 v70, v70, v75
	v_bitop3_b32 v71, v71, v74, s67 bitop3:0x78
	v_cmp_class_f32_e64 vcc, v1, s68
	v_lshlrev_b32_e32 v250, 16, v82
	v_and_b32_e32 v251, 0xffff0000, v82
	v_cndmask_b32_e32 v98, v245, v71, vcc
	v_cndmask_b32_e32 v163, v245, v70, vcc
	global_load_dwordx4 v[70:73], v[102:103], off offset:48
	global_load_dwordx4 v[74:77], v[102:103], off offset:32
	v_lshlrev_b32_e32 v206, 16, v83
	v_and_b32_e32 v207, 0xffff0000, v83
	v_pk_mul_f32 v[82:83], v[250:251], v[250:251]
	v_pk_mul_f32 v[172:173], v[206:207], v[206:207]
	v_add_f32_e32 v1, v82, v83
	v_lshlrev_b32_e32 v204, 16, v84
	v_and_b32_e32 v205, 0xffff0000, v84
	v_add_f32_e32 v1, v172, v1
	v_lshlrev_b32_e32 v202, 16, v85
	v_and_b32_e32 v203, 0xffff0000, v85
	v_pk_mul_f32 v[84:85], v[204:205], v[204:205]
	v_add_f32_e32 v1, v173, v1
	v_add_f32_e32 v1, v84, v1
	v_pk_mul_f32 v[170:171], v[202:203], v[202:203]
	v_add_f32_e32 v1, v85, v1
	v_lshlrev_b32_e32 v200, 16, v86
	v_and_b32_e32 v201, 0xffff0000, v86
	v_add_f32_e32 v1, v170, v1
	v_lshlrev_b32_e32 v198, 16, v87
	v_and_b32_e32 v199, 0xffff0000, v87
	v_pk_mul_f32 v[86:87], v[200:201], v[200:201]
	v_add_f32_e32 v1, v171, v1
	v_add_f32_e32 v1, v86, v1
	v_pk_mul_f32 v[168:169], v[198:199], v[198:199]
	v_add_f32_e32 v1, v87, v1
	v_lshlrev_b32_e32 v196, 16, v88
	v_and_b32_e32 v197, 0xffff0000, v88
	v_add_f32_e32 v1, v168, v1
	v_lshlrev_b32_e32 v194, 16, v89
	v_and_b32_e32 v195, 0xffff0000, v89
	v_pk_mul_f32 v[88:89], v[196:197], v[196:197]
	v_add_f32_e32 v1, v169, v1
	v_add_f32_e32 v1, v88, v1
	v_pk_mul_f32 v[166:167], v[194:195], v[194:195]
	v_add_f32_e32 v1, v89, v1
	v_add_f32_e32 v1, v166, v1
	v_add_f32_e32 v1, v167, v1
	s_nop 1
	v_mov_b32_dpp v82, v1 quad_perm:[1,0,3,2] row_mask:0xf bank_mask:0xf
	ds_bpermute_b32 v192, v216, v98
	ds_bpermute_b32 v193, v216, v163
	ds_bpermute_b32 v190, v217, v98
	ds_bpermute_b32 v191, v217, v163
	s_waitcnt lgkmcnt(4)
	v_add_f32_e32 v1, v1, v82
	ds_bpermute_b32 v82, v209, v1
	ds_bpermute_b32 v188, v218, v98
	ds_bpermute_b32 v189, v218, v163
	ds_bpermute_b32 v186, v219, v98
	ds_bpermute_b32 v187, v219, v163
	s_waitcnt lgkmcnt(4)
	v_add_f32_e32 v1, v1, v82
	ds_bpermute_b32 v82, v210, v1
	ds_bpermute_b32 v184, v220, v98
	ds_bpermute_b32 v185, v220, v163
	ds_bpermute_b32 v182, v221, v98
	ds_bpermute_b32 v183, v221, v163
	s_waitcnt lgkmcnt(4)
	v_add_f32_e32 v1, v1, v82
	v_fmamk_f32 v1, v1, 0x3c000000, v95
	v_mul_f32_e32 v82, 0x4b800000, v1
	v_cmp_gt_f32_e32 vcc, s50, v1
	ds_bpermute_b32 v180, v222, v98
	ds_bpermute_b32 v181, v222, v163
	v_cndmask_b32_e32 v1, v1, v82, vcc
	v_rsq_f32_e32 v1, v1
	ds_bpermute_b32 v178, v223, v98
	ds_bpermute_b32 v179, v223, v163
	ds_bpermute_b32 v176, v224, v98
	v_mul_f32_e32 v82, 0x45800000, v1
	v_cndmask_b32_e32 v84, v1, v82, vcc
	v_mov_b32_e32 v85, v84
	v_pk_mul_f32 v[82:83], v[84:85], v[250:251] op_sel_hi:[0,1]
	s_waitcnt vmcnt(2)
	v_pk_mul_f32 v[82:83], v[90:91], v[82:83]
	ds_bpermute_b32 v177, v224, v163
	ds_bpermute_b32 v174, v225, v98
	ds_bpermute_b32 v175, v225, v163
	ds_bpermute_b32 v172, v226, v98
	ds_bpermute_b32 v173, v226, v163
	ds_bpermute_b32 v170, v227, v98
	ds_bpermute_b32 v171, v227, v163
	ds_bpermute_b32 v168, v228, v98
	ds_bpermute_b32 v169, v228, v163
	ds_bpermute_b32 v166, v229, v98
	ds_bpermute_b32 v167, v229, v163
	ds_bpermute_b32 v88, v230, v98
	ds_bpermute_b32 v89, v230, v163
	ds_bpermute_b32 v86, v231, v98
	ds_bpermute_b32 v87, v231, v163
	s_nop 1
	v_mov_b32_dpp v91, v82 quad_perm:[1,0,3,2] row_mask:0xf bank_mask:0xf
	v_cmp_lt_i32_e32 vcc, 0, v96
	s_and_saveexec_b64 s[2:3], vcc
	s_xor_b64 s[2:3], exec, s[2:3]
	s_cbranch_execz .LBB0_567
	v_cmp_eq_u32_e32 vcc, 1, v96
	s_and_saveexec_b64 s[10:11], vcc
	s_cbranch_execz .LBB0_566
	v_mov_b32_e32 v90, v82
	s_waitcnt lgkmcnt(0)
	v_pk_mul_f32 v[90:91], v[90:91], v[192:193]
	s_nop 0
	v_add_f32_e32 v82, v90, v91

.LBB0_569:
	s_or_b64 exec, exec, s[2:3]
	s_waitcnt lgkmcnt(0)
	s_nop 1
	v_mov_b32_dpp v91, v83 quad_perm:[1,0,3,2] row_mask:0xf bank_mask:0xf
	v_cmp_lt_i32_e32 vcc, 0, v96
	s_and_saveexec_b64 s[2:3], vcc
	s_xor_b64 s[2:3], exec, s[2:3]
	s_cbranch_execz .LBB0_573
	v_cmp_eq_u32_e32 vcc, 1, v96
	s_and_saveexec_b64 s[10:11], vcc
	s_cbranch_execz .LBB0_572
	v_mov_b32_e32 v250, v83
	v_mov_b32_e32 v251, v191
	v_mov_b32_e32 v90, v190
	v_mul_f32_e32 v252, v83, v190
	s_waitcnt lgkmcnt(0)
	v_pk_fma_f32 v[90:91], v[250:251], v[90:91], v[252:253] op_sel_hi:[1,1,0]
	s_nop 0
	v_mov_b32_e32 v83, v91

.LBB0_575:
	s_or_b64 exec, exec, s[2:3]
	s_waitcnt lgkmcnt(0)
	v_pk_mul_f32 v[90:91], v[84:85], v[206:207]
	v_cmp_lt_i32_e32 vcc, 0, v96
	v_pk_mul_f32 v[90:91], v[92:93], v[90:91]
	s_nop 1
	v_mov_b32_dpp v93, v90 quad_perm:[1,0,3,2] row_mask:0xf bank_mask:0xf
	s_and_saveexec_b64 s[2:3], vcc
	s_xor_b64 s[2:3], exec, s[2:3]
	s_cbranch_execz .LBB0_579
	v_cmp_eq_u32_e32 vcc, 1, v96
	s_and_saveexec_b64 s[10:11], vcc
	s_cbranch_execz .LBB0_578
	v_mov_b32_e32 v92, v90
	s_waitcnt lgkmcnt(0)
	v_pk_mul_f32 v[92:93], v[92:93], v[188:189]
	s_nop 0
	v_add_f32_e32 v90, v92, v93

.LBB0_581:
	s_or_b64 exec, exec, s[2:3]
	s_waitcnt lgkmcnt(0)
	s_nop 1
	v_mov_b32_dpp v93, v91 quad_perm:[1,0,3,2] row_mask:0xf bank_mask:0xf
	v_cmp_lt_i32_e32 vcc, 0, v96
	s_and_saveexec_b64 s[2:3], vcc
	s_xor_b64 s[2:3], exec, s[2:3]
	s_cbranch_execz .LBB0_585
	v_cmp_eq_u32_e32 vcc, 1, v96
	s_and_saveexec_b64 s[10:11], vcc
	s_cbranch_execz .LBB0_584
	v_mov_b32_e32 v206, v91
	v_mov_b32_e32 v207, v187
	v_mov_b32_e32 v92, v186
	v_mul_f32_e32 v250, v91, v186
	s_waitcnt lgkmcnt(0)
	v_pk_fma_f32 v[92:93], v[206:207], v[92:93], v[250:251] op_sel_hi:[1,1,0]
	s_nop 0
	v_mov_b32_e32 v91, v93

.LBB0_587:
	s_or_b64 exec, exec, s[2:3]
	s_waitcnt lgkmcnt(0)
	v_pk_mul_f32 v[92:93], v[84:85], v[204:205]
	v_cmp_lt_i32_e32 vcc, 0, v96
	v_pk_mul_f32 v[78:79], v[78:79], v[92:93]
	s_nop 1
	v_mov_b32_dpp v93, v78 quad_perm:[1,0,3,2] row_mask:0xf bank_mask:0xf
	s_and_saveexec_b64 s[2:3], vcc
	s_xor_b64 s[2:3], exec, s[2:3]
	s_cbranch_execz .LBB0_591
	v_cmp_eq_u32_e32 vcc, 1, v96
	s_and_saveexec_b64 s[10:11], vcc
	s_cbranch_execz .LBB0_590
	v_mov_b32_e32 v92, v78
	s_waitcnt lgkmcnt(0)
	v_pk_mul_f32 v[92:93], v[92:93], v[184:185]
	s_nop 0
	v_add_f32_e32 v78, v92, v93

.LBB0_593:
	s_or_b64 exec, exec, s[2:3]
	s_waitcnt lgkmcnt(0)
	s_nop 1
	v_mov_b32_dpp v93, v79 quad_perm:[1,0,3,2] row_mask:0xf bank_mask:0xf
	v_cmp_lt_i32_e32 vcc, 0, v96
	s_and_saveexec_b64 s[2:3], vcc
	s_xor_b64 s[2:3], exec, s[2:3]
	s_cbranch_execz .LBB0_597
	v_cmp_eq_u32_e32 vcc, 1, v96
	s_and_saveexec_b64 s[10:11], vcc
	s_cbranch_execz .LBB0_596
	v_mov_b32_e32 v204, v79
	v_mov_b32_e32 v205, v183
	v_mov_b32_e32 v92, v182
	v_mul_f32_e32 v206, v79, v182
	s_waitcnt lgkmcnt(0)
	v_pk_fma_f32 v[92:93], v[204:205], v[92:93], v[206:207] op_sel_hi:[1,1,0]
	s_nop 0
	v_mov_b32_e32 v79, v93

.LBB0_599:
	s_or_b64 exec, exec, s[2:3]
	s_waitcnt lgkmcnt(0)
	v_pk_mul_f32 v[92:93], v[84:85], v[202:203]
	v_cmp_lt_i32_e32 vcc, 0, v96
	v_pk_mul_f32 v[80:81], v[80:81], v[92:93]
	s_nop 1
	v_mov_b32_dpp v93, v80 quad_perm:[1,0,3,2] row_mask:0xf bank_mask:0xf
	s_and_saveexec_b64 s[2:3], vcc
	s_xor_b64 s[2:3], exec, s[2:3]
	s_cbranch_execz .LBB0_603
	v_cmp_eq_u32_e32 vcc, 1, v96
	s_and_saveexec_b64 s[10:11], vcc
	s_cbranch_execz .LBB0_602
	v_mov_b32_e32 v92, v80
	s_waitcnt lgkmcnt(0)
	v_pk_mul_f32 v[92:93], v[92:93], v[180:181]
	s_nop 0
	v_add_f32_e32 v80, v92, v93

.LBB0_605:
	s_or_b64 exec, exec, s[2:3]
	s_waitcnt lgkmcnt(0)
	s_nop 1
	v_mov_b32_dpp v93, v81 quad_perm:[1,0,3,2] row_mask:0xf bank_mask:0xf
	v_cmp_lt_i32_e32 vcc, 0, v96
	s_and_saveexec_b64 s[2:3], vcc
	s_xor_b64 s[2:3], exec, s[2:3]
	s_cbranch_execz .LBB0_609
	v_cmp_eq_u32_e32 vcc, 1, v96
	s_and_saveexec_b64 s[10:11], vcc
	s_cbranch_execz .LBB0_608
	v_mov_b32_e32 v202, v81
	v_mov_b32_e32 v203, v179
	v_mov_b32_e32 v92, v178
	v_mul_f32_e32 v204, v81, v178
	s_waitcnt lgkmcnt(0)
	v_pk_fma_f32 v[92:93], v[202:203], v[92:93], v[204:205] op_sel_hi:[1,1,0]
	s_nop 0
	v_mov_b32_e32 v81, v93

.LBB0_611:
	s_or_b64 exec, exec, s[2:3]
	s_waitcnt lgkmcnt(0)
	v_pk_mul_f32 v[92:93], v[84:85], v[200:201]
	v_cmp_lt_i32_e32 vcc, 0, v96
	s_waitcnt vmcnt(0)
	v_pk_mul_f32 v[74:75], v[74:75], v[92:93]
	s_nop 1
	v_mov_b32_dpp v93, v74 quad_perm:[1,0,3,2] row_mask:0xf bank_mask:0xf
	s_and_saveexec_b64 s[2:3], vcc
	s_xor_b64 s[2:3], exec, s[2:3]
	s_cbranch_execz .LBB0_615
	v_cmp_eq_u32_e32 vcc, 1, v96
	s_and_saveexec_b64 s[10:11], vcc
	s_cbranch_execz .LBB0_614
	v_mov_b32_e32 v92, v74
	s_waitcnt lgkmcnt(0)
	v_pk_mul_f32 v[92:93], v[92:93], v[176:177]
	s_nop 0
	v_add_f32_e32 v74, v92, v93

.LBB0_617:
	s_or_b64 exec, exec, s[2:3]
	s_waitcnt lgkmcnt(0)
	s_nop 1
	v_mov_b32_dpp v93, v75 quad_perm:[1,0,3,2] row_mask:0xf bank_mask:0xf
	v_cmp_lt_i32_e32 vcc, 0, v96
	s_and_saveexec_b64 s[2:3], vcc
	s_xor_b64 s[2:3], exec, s[2:3]
	s_cbranch_execz .LBB0_621
	v_cmp_eq_u32_e32 vcc, 1, v96
	s_and_saveexec_b64 s[10:11], vcc
	s_cbranch_execz .LBB0_620
	v_mov_b32_e32 v200, v75
	v_mov_b32_e32 v201, v175
	v_mov_b32_e32 v92, v174
	v_mul_f32_e32 v202, v75, v174
	s_waitcnt lgkmcnt(0)
	v_pk_fma_f32 v[92:93], v[200:201], v[92:93], v[202:203] op_sel_hi:[1,1,0]
	s_nop 0
	v_mov_b32_e32 v75, v93

.LBB0_623:
	s_or_b64 exec, exec, s[2:3]
	s_waitcnt lgkmcnt(0)
	v_pk_mul_f32 v[92:93], v[84:85], v[198:199]
	v_cmp_lt_i32_e32 vcc, 0, v96
	v_pk_mul_f32 v[76:77], v[92:93], v[76:77]
	s_nop 1
	v_mov_b32_dpp v93, v76 quad_perm:[1,0,3,2] row_mask:0xf bank_mask:0xf
	s_and_saveexec_b64 s[2:3], vcc
	s_xor_b64 s[2:3], exec, s[2:3]
	s_cbranch_execz .LBB0_627
	v_cmp_eq_u32_e32 vcc, 1, v96
	s_and_saveexec_b64 s[10:11], vcc
	s_cbranch_execz .LBB0_626
	v_mov_b32_e32 v92, v76
	s_waitcnt lgkmcnt(0)
	v_pk_mul_f32 v[92:93], v[92:93], v[172:173]
	s_nop 0
	v_add_f32_e32 v76, v92, v93

.LBB0_629:
	s_or_b64 exec, exec, s[2:3]
	s_waitcnt lgkmcnt(0)
	s_nop 1
	v_mov_b32_dpp v93, v77 quad_perm:[1,0,3,2] row_mask:0xf bank_mask:0xf
	v_cmp_lt_i32_e32 vcc, 0, v96
	s_and_saveexec_b64 s[2:3], vcc
	s_xor_b64 s[2:3], exec, s[2:3]
	s_cbranch_execz .LBB0_633
	v_cmp_eq_u32_e32 vcc, 1, v96
	s_and_saveexec_b64 s[10:11], vcc
	s_cbranch_execz .LBB0_632
	v_mov_b32_e32 v198, v77
	v_mov_b32_e32 v199, v171
	v_mov_b32_e32 v92, v170
	v_mul_f32_e32 v200, v77, v170
	s_waitcnt lgkmcnt(0)
	v_pk_fma_f32 v[92:93], v[198:199], v[92:93], v[200:201] op_sel_hi:[1,1,0]
	s_nop 0
	v_mov_b32_e32 v77, v93

.LBB0_635:
	s_or_b64 exec, exec, s[2:3]
	s_waitcnt lgkmcnt(0)
	v_pk_mul_f32 v[92:93], v[84:85], v[196:197]
	v_cmp_lt_i32_e32 vcc, 0, v96
	v_pk_mul_f32 v[70:71], v[92:93], v[70:71]
	s_nop 1
	v_mov_b32_dpp v93, v70 quad_perm:[1,0,3,2] row_mask:0xf bank_mask:0xf
	s_and_saveexec_b64 s[2:3], vcc
	s_xor_b64 s[2:3], exec, s[2:3]
	s_cbranch_execz .LBB0_639
	v_cmp_eq_u32_e32 vcc, 1, v96
	s_and_saveexec_b64 s[10:11], vcc
	s_cbranch_execz .LBB0_638
	v_mov_b32_e32 v92, v70
	s_waitcnt lgkmcnt(0)
	v_pk_mul_f32 v[92:93], v[92:93], v[168:169]
	s_nop 0
	v_add_f32_e32 v70, v92, v93

.LBB0_641:
	s_or_b64 exec, exec, s[2:3]
	s_waitcnt lgkmcnt(0)
	s_nop 1
	v_mov_b32_dpp v93, v71 quad_perm:[1,0,3,2] row_mask:0xf bank_mask:0xf
	v_cmp_lt_i32_e32 vcc, 0, v96
	s_and_saveexec_b64 s[2:3], vcc
	s_xor_b64 s[2:3], exec, s[2:3]
	s_cbranch_execz .LBB0_645
	v_cmp_eq_u32_e32 vcc, 1, v96
	s_and_saveexec_b64 s[10:11], vcc
	s_cbranch_execz .LBB0_644
	v_mov_b32_e32 v196, v71
	v_mov_b32_e32 v197, v167
	v_mov_b32_e32 v92, v166
	v_mul_f32_e32 v198, v71, v166
	s_waitcnt lgkmcnt(0)
	v_pk_fma_f32 v[92:93], v[196:197], v[92:93], v[198:199] op_sel_hi:[1,1,0]
	s_nop 0
	v_mov_b32_e32 v71, v93

.LBB0_647:
	s_or_b64 exec, exec, s[2:3]
	v_pk_mul_f32 v[84:85], v[84:85], v[194:195]
	v_cmp_lt_i32_e32 vcc, 0, v96
	v_pk_mul_f32 v[72:73], v[84:85], v[72:73]
	s_nop 1
	v_mov_b32_dpp v85, v72 quad_perm:[1,0,3,2] row_mask:0xf bank_mask:0xf
	s_and_saveexec_b64 s[2:3], vcc
	s_xor_b64 s[2:3], exec, s[2:3]
	s_cbranch_execz .LBB0_651
	v_cmp_eq_u32_e32 vcc, 1, v96
	s_and_saveexec_b64 s[10:11], vcc
	s_cbranch_execz .LBB0_650
	v_mov_b32_e32 v84, v72
	s_waitcnt lgkmcnt(0)
	v_pk_mul_f32 v[84:85], v[84:85], v[88:89]
	s_nop 0
	v_add_f32_e32 v72, v84, v85

.LBB0_653:
	s_or_b64 exec, exec, s[2:3]
	s_waitcnt lgkmcnt(0)
	s_nop 1
	v_mov_b32_dpp v85, v73 quad_perm:[1,0,3,2] row_mask:0xf bank_mask:0xf
	v_cmp_lt_i32_e32 vcc, 0, v96
	s_and_saveexec_b64 s[2:3], vcc
	s_xor_b64 s[2:3], exec, s[2:3]
	s_cbranch_execz .LBB0_657
	v_cmp_eq_u32_e32 vcc, 1, v96
	s_and_saveexec_b64 s[10:11], vcc
	s_cbranch_execz .LBB0_656
	v_mov_b32_e32 v92, v73
	v_mov_b32_e32 v93, v87
	v_mov_b32_e32 v84, v86
	v_mul_f32_e32 v194, v73, v86
	s_waitcnt lgkmcnt(0)
	v_pk_fma_f32 v[84:85], v[92:93], v[84:85], v[194:195] op_sel_hi:[1,1,0]
	s_nop 0
	v_mov_b32_e32 v73, v85

.LBB0_659:
	s_or_b64 exec, exec, s[2:3]
	v_lshl_add_u64 v[92:93], s[88:89], 0, v[146:147]
	v_cvt_pk_bf16_f32 v74, v74, v75
	v_cvt_pk_bf16_f32 v75, v76, v77
	v_cvt_pk_bf16_f32 v76, v70, v71
	v_add_co_u32_e32 v70, vcc, s69, v92
	v_cvt_pk_bf16_f32 v82, v82, v83
	v_cvt_pk_bf16_f32 v83, v90, v91
	v_cvt_pk_bf16_f32 v84, v78, v79
	s_waitcnt lgkmcnt(0)
	v_cvt_pk_bf16_f32 v85, v80, v81
	v_addc_co_u32_e32 v71, vcc, 0, v93, vcc
	v_cvt_pk_bf16_f32 v77, v72, v73
	global_store_dwordx4 v[70:71], v[82:85], off
	global_store_dwordx4 v[70:71], v[74:77], off offset:16
	global_load_dwordx4 v[82:85], v[104:105], off
	s_nop 0
	global_load_dwordx4 v[78:81], v[104:105], off offset:16
	global_load_dwordx4 v[70:73], v[104:105], off offset:48
	global_load_dwordx4 v[74:77], v[104:105], off offset:32
	v_lshlrev_b32_e32 v90, 16, v66
	v_and_b32_e32 v91, 0xffff0000, v66
	v_pk_mul_f32 v[92:93], v[90:91], v[90:91]
	v_lshlrev_b32_e32 v66, 16, v67
	v_and_b32_e32 v67, 0xffff0000, v67
	v_pk_mul_f32 v[202:203], v[66:67], v[66:67]
	v_add_f32_e32 v1, v92, v93
	v_lshlrev_b32_e32 v194, 16, v68
	v_and_b32_e32 v195, 0xffff0000, v68
	v_add_f32_e32 v1, v202, v1
	v_pk_mul_f32 v[204:205], v[194:195], v[194:195]
	v_add_f32_e32 v1, v203, v1
	v_lshlrev_b32_e32 v68, 16, v69
	v_and_b32_e32 v69, 0xffff0000, v69
	v_add_f32_e32 v1, v204, v1
	v_pk_mul_f32 v[206:207], v[68:69], v[68:69]
	v_add_f32_e32 v1, v205, v1
	v_lshlrev_b32_e32 v196, 16, v62
	v_and_b32_e32 v197, 0xffff0000, v62
	v_add_f32_e32 v1, v206, v1
	v_pk_mul_f32 v[250:251], v[196:197], v[196:197]
	v_add_f32_e32 v1, v207, v1
	v_lshlrev_b32_e32 v62, 16, v63
	v_and_b32_e32 v63, 0xffff0000, v63
	v_add_f32_e32 v1, v250, v1
	v_pk_mul_f32 v[252:253], v[62:63], v[62:63]
	v_add_f32_e32 v1, v251, v1
	v_lshlrev_b32_e32 v198, 16, v64
	v_and_b32_e32 v199, 0xffff0000, v64
	v_add_f32_e32 v1, v252, v1
	v_pk_mul_f32 v[240:241], v[198:199], v[198:199]
	v_add_f32_e32 v1, v253, v1
	v_lshlrev_b32_e32 v200, 16, v65
	v_and_b32_e32 v201, 0xffff0000, v65
	v_add_f32_e32 v1, v240, v1
	v_pk_mul_f32 v[64:65], v[200:201], v[200:201]
	v_add_f32_e32 v1, v241, v1
	v_add_f32_e32 v1, v64, v1
	v_add_f32_e32 v1, v65, v1
	s_nop 1
	v_mov_b32_dpp v64, v1 quad_perm:[1,0,3,2] row_mask:0xf bank_mask:0xf
	s_waitcnt lgkmcnt(0)
	v_add_f32_e32 v1, v1, v64
	ds_bpermute_b32 v64, v209, v1
	s_waitcnt lgkmcnt(0)
	v_add_f32_e32 v1, v1, v64
	ds_bpermute_b32 v64, v210, v1
	s_waitcnt lgkmcnt(0)
	v_add_f32_e32 v1, v1, v64
	v_fmamk_f32 v1, v1, 0x3c000000, v95
	v_mul_f32_e32 v64, 0x4b800000, v1
	v_cmp_gt_f32_e32 vcc, s50, v1
	s_nop 1
	v_cndmask_b32_e32 v1, v1, v64, vcc
	v_rsq_f32_e32 v1, v1
	s_nop 0
	v_mul_f32_e32 v64, 0x45800000, v1
	v_cndmask_b32_e32 v202, v1, v64, vcc
	v_mov_b32_e32 v203, v202
	v_pk_mul_f32 v[64:65], v[202:203], v[90:91] op_sel_hi:[0,1]
	v_pk_mul_f32 v[62:63], v[202:203], v[62:63]
	v_cmp_lt_i32_e32 vcc, 0, v96
	s_waitcnt vmcnt(3)
	v_pk_mul_f32 v[82:83], v[82:83], v[64:65]
	v_pk_mul_f32 v[64:65], v[202:203], v[66:67]
	s_nop 1
	v_mov_b32_dpp v93, v82 quad_perm:[1,0,3,2] row_mask:0xf bank_mask:0xf
	v_pk_mul_f32 v[90:91], v[84:85], v[64:65]
	v_pk_mul_f32 v[64:65], v[202:203], v[194:195]
	s_waitcnt vmcnt(0)
	v_pk_mul_f32 v[66:67], v[62:63], v[76:77]
	v_pk_mul_f32 v[84:85], v[78:79], v[64:65]
	v_pk_mul_f32 v[64:65], v[202:203], v[68:69]
	v_pk_mul_f32 v[62:63], v[202:203], v[198:199]
	v_pk_mul_f32 v[78:79], v[80:81], v[64:65]
	v_pk_mul_f32 v[64:65], v[202:203], v[196:197]
	s_nop 0
	v_pk_mul_f32 v[68:69], v[74:75], v[64:65]
	v_pk_mul_f32 v[64:65], v[62:63], v[70:71]
	v_pk_mul_f32 v[62:63], v[202:203], v[200:201]
	s_nop 0
	v_pk_mul_f32 v[62:63], v[62:63], v[72:73]
	s_and_saveexec_b64 s[2:3], vcc
	s_xor_b64 s[2:3], exec, s[2:3]
	s_cbranch_execz .LBB0_663
	v_cmp_eq_u32_e32 vcc, 1, v96
	s_and_saveexec_b64 s[10:11], vcc
	s_cbranch_execz .LBB0_662
	v_mov_b32_e32 v92, v82
	s_waitcnt lgkmcnt(0)
	v_pk_mul_f32 v[70:71], v[92:93], v[192:193]
	s_nop 0
	v_add_f32_e32 v82, v70, v71

.LBB0_665:
	s_or_b64 exec, exec, s[2:3]
	s_nop 1
	v_mov_b32_dpp v71, v83 quad_perm:[1,0,3,2] row_mask:0xf bank_mask:0xf
	v_cmp_lt_i32_e32 vcc, 0, v96
	s_and_saveexec_b64 s[2:3], vcc
	s_xor_b64 s[2:3], exec, s[2:3]
	s_cbranch_execz .LBB0_669
	v_cmp_eq_u32_e32 vcc, 1, v96
	s_and_saveexec_b64 s[10:11], vcc
	s_cbranch_execz .LBB0_668
	v_mov_b32_e32 v70, v83
	v_mul_f32_e32 v72, v83, v190
	s_waitcnt lgkmcnt(0)
	v_pk_fma_f32 v[70:71], v[70:71], v[190:191], v[72:73] op_sel_hi:[1,1,0]
	s_nop 0
	v_mov_b32_e32 v83, v71

.LBB0_671:
	s_or_b64 exec, exec, s[2:3]
	s_waitcnt lgkmcnt(0)
	s_nop 1
	v_mov_b32_dpp v71, v90 quad_perm:[1,0,3,2] row_mask:0xf bank_mask:0xf
	v_cmp_lt_i32_e32 vcc, 0, v96
	s_and_saveexec_b64 s[2:3], vcc
	s_xor_b64 s[2:3], exec, s[2:3]
	s_cbranch_execz .LBB0_675
	v_cmp_eq_u32_e32 vcc, 1, v96
	s_and_saveexec_b64 s[10:11], vcc
	s_cbranch_execz .LBB0_674
	v_mov_b32_e32 v70, v90
	s_waitcnt lgkmcnt(0)
	v_pk_mul_f32 v[70:71], v[70:71], v[188:189]
	s_nop 0
	v_add_f32_e32 v90, v70, v71

.LBB0_677:
	s_or_b64 exec, exec, s[2:3]
	s_waitcnt lgkmcnt(0)
	s_nop 1
	v_mov_b32_dpp v71, v91 quad_perm:[1,0,3,2] row_mask:0xf bank_mask:0xf
	v_cmp_lt_i32_e32 vcc, 0, v96
	s_and_saveexec_b64 s[2:3], vcc
	s_xor_b64 s[2:3], exec, s[2:3]
	s_cbranch_execz .LBB0_681
	v_cmp_eq_u32_e32 vcc, 1, v96
	s_and_saveexec_b64 s[10:11], vcc
	s_cbranch_execz .LBB0_680
	v_mov_b32_e32 v70, v91
	s_waitcnt lgkmcnt(0)
	v_mul_f32_e32 v72, v71, v187
	v_pk_fma_f32 v[70:71], v[70:71], v[186:187], v[72:73] op_sel_hi:[1,1,0]
	s_nop 0
	v_mov_b32_e32 v91, v70

.LBB0_683:
	s_or_b64 exec, exec, s[2:3]
	s_waitcnt lgkmcnt(0)
	s_nop 1
	v_mov_b32_dpp v71, v84 quad_perm:[1,0,3,2] row_mask:0xf bank_mask:0xf
	v_cmp_lt_i32_e32 vcc, 0, v96
	s_and_saveexec_b64 s[2:3], vcc
	s_xor_b64 s[2:3], exec, s[2:3]
	s_cbranch_execz .LBB0_687
	v_cmp_eq_u32_e32 vcc, 1, v96
	s_and_saveexec_b64 s[10:11], vcc
	s_cbranch_execz .LBB0_686
	v_mov_b32_e32 v70, v84
	s_waitcnt lgkmcnt(0)
	v_pk_mul_f32 v[70:71], v[70:71], v[184:185]
	s_nop 0
	v_add_f32_e32 v84, v70, v71

.LBB0_689:
	s_or_b64 exec, exec, s[2:3]
	s_waitcnt lgkmcnt(0)
	s_nop 1
	v_mov_b32_dpp v71, v85 quad_perm:[1,0,3,2] row_mask:0xf bank_mask:0xf
	v_cmp_lt_i32_e32 vcc, 0, v96
	s_and_saveexec_b64 s[2:3], vcc
	s_xor_b64 s[2:3], exec, s[2:3]
	s_cbranch_execz .LBB0_693
	v_cmp_eq_u32_e32 vcc, 1, v96
	s_and_saveexec_b64 s[10:11], vcc
	s_cbranch_execz .LBB0_692
	v_mov_b32_e32 v70, v85
	s_waitcnt lgkmcnt(0)
	v_mul_f32_e32 v72, v71, v183
	v_pk_fma_f32 v[70:71], v[70:71], v[182:183], v[72:73] op_sel_hi:[1,1,0]
	s_nop 0
	v_mov_b32_e32 v85, v70

.LBB0_695:
	s_or_b64 exec, exec, s[2:3]
	s_waitcnt lgkmcnt(0)
	s_nop 1
	v_mov_b32_dpp v71, v78 quad_perm:[1,0,3,2] row_mask:0xf bank_mask:0xf
	v_cmp_lt_i32_e32 vcc, 0, v96
	s_and_saveexec_b64 s[2:3], vcc
	s_xor_b64 s[2:3], exec, s[2:3]
	s_cbranch_execz .LBB0_699
	v_cmp_eq_u32_e32 vcc, 1, v96
	s_and_saveexec_b64 s[10:11], vcc
	s_cbranch_execz .LBB0_698
	v_mov_b32_e32 v70, v78
	s_waitcnt lgkmcnt(0)
	v_pk_mul_f32 v[70:71], v[70:71], v[180:181]
	s_nop 0
	v_add_f32_e32 v78, v70, v71

.LBB0_701:
	s_or_b64 exec, exec, s[2:3]
	s_waitcnt lgkmcnt(0)
	s_nop 1
	v_mov_b32_dpp v71, v79 quad_perm:[1,0,3,2] row_mask:0xf bank_mask:0xf
	v_cmp_lt_i32_e32 vcc, 0, v96
	s_and_saveexec_b64 s[2:3], vcc
	s_xor_b64 s[2:3], exec, s[2:3]
	s_cbranch_execz .LBB0_705
	v_cmp_eq_u32_e32 vcc, 1, v96
	s_and_saveexec_b64 s[10:11], vcc
	s_cbranch_execz .LBB0_704
	v_mov_b32_e32 v70, v79
	s_waitcnt lgkmcnt(0)
	v_mul_f32_e32 v72, v71, v179
	v_pk_fma_f32 v[70:71], v[70:71], v[178:179], v[72:73] op_sel_hi:[1,1,0]
	s_nop 0
	v_mov_b32_e32 v79, v70

.LBB0_707:
	s_or_b64 exec, exec, s[2:3]
	s_waitcnt lgkmcnt(0)
	s_nop 1
	v_mov_b32_dpp v71, v68 quad_perm:[1,0,3,2] row_mask:0xf bank_mask:0xf
	v_cmp_lt_i32_e32 vcc, 0, v96
	s_and_saveexec_b64 s[2:3], vcc
	s_xor_b64 s[2:3], exec, s[2:3]
	s_cbranch_execz .LBB0_711
	v_cmp_eq_u32_e32 vcc, 1, v96
	s_and_saveexec_b64 s[10:11], vcc
	s_cbranch_execz .LBB0_710
	v_mov_b32_e32 v70, v68
	s_waitcnt lgkmcnt(0)
	v_pk_mul_f32 v[70:71], v[70:71], v[176:177]
	s_nop 0
	v_add_f32_e32 v68, v70, v71

.LBB0_713:
	s_or_b64 exec, exec, s[2:3]
	s_waitcnt lgkmcnt(0)
	s_nop 1
	v_mov_b32_dpp v71, v69 quad_perm:[1,0,3,2] row_mask:0xf bank_mask:0xf
	v_cmp_lt_i32_e32 vcc, 0, v96
	s_and_saveexec_b64 s[2:3], vcc
	s_xor_b64 s[2:3], exec, s[2:3]
	s_cbranch_execz .LBB0_717
	v_cmp_eq_u32_e32 vcc, 1, v96
	s_and_saveexec_b64 s[10:11], vcc
	s_cbranch_execz .LBB0_716
	v_mov_b32_e32 v70, v69
	s_waitcnt lgkmcnt(0)
	v_mul_f32_e32 v72, v71, v175
	v_pk_fma_f32 v[70:71], v[70:71], v[174:175], v[72:73] op_sel_hi:[1,1,0]
	s_nop 0
	v_mov_b32_e32 v69, v70

.LBB0_719:
	s_or_b64 exec, exec, s[2:3]
	s_waitcnt lgkmcnt(0)
	s_nop 1
	v_mov_b32_dpp v71, v66 quad_perm:[1,0,3,2] row_mask:0xf bank_mask:0xf
	v_cmp_lt_i32_e32 vcc, 0, v96
	s_and_saveexec_b64 s[2:3], vcc
	s_xor_b64 s[2:3], exec, s[2:3]
	s_cbranch_execz .LBB0_723
	v_cmp_eq_u32_e32 vcc, 1, v96
	s_and_saveexec_b64 s[10:11], vcc
	s_cbranch_execz .LBB0_722
	v_mov_b32_e32 v70, v66
	s_waitcnt lgkmcnt(0)
	v_pk_mul_f32 v[70:71], v[70:71], v[172:173]
	s_nop 0
	v_add_f32_e32 v66, v70, v71

.LBB0_725:
	s_or_b64 exec, exec, s[2:3]
	s_waitcnt lgkmcnt(0)
	s_nop 1
	v_mov_b32_dpp v71, v67 quad_perm:[1,0,3,2] row_mask:0xf bank_mask:0xf
	v_cmp_lt_i32_e32 vcc, 0, v96
	s_and_saveexec_b64 s[2:3], vcc
	s_xor_b64 s[2:3], exec, s[2:3]
	s_cbranch_execz .LBB0_729
	v_cmp_eq_u32_e32 vcc, 1, v96
	s_and_saveexec_b64 s[10:11], vcc
	s_cbranch_execz .LBB0_728
	v_mov_b32_e32 v70, v67
	s_waitcnt lgkmcnt(0)
	v_mul_f32_e32 v72, v71, v171
	v_pk_fma_f32 v[70:71], v[70:71], v[170:171], v[72:73] op_sel_hi:[1,1,0]
	s_nop 0
	v_mov_b32_e32 v67, v70

.LBB0_731:
	s_or_b64 exec, exec, s[2:3]
	s_waitcnt lgkmcnt(0)
	s_nop 1
	v_mov_b32_dpp v71, v64 quad_perm:[1,0,3,2] row_mask:0xf bank_mask:0xf
	v_cmp_lt_i32_e32 vcc, 0, v96
	s_and_saveexec_b64 s[2:3], vcc
	s_xor_b64 s[2:3], exec, s[2:3]
	s_cbranch_execz .LBB0_735
	v_cmp_eq_u32_e32 vcc, 1, v96
	s_and_saveexec_b64 s[10:11], vcc
	s_cbranch_execz .LBB0_734
	v_mov_b32_e32 v70, v64
	s_waitcnt lgkmcnt(0)
	v_pk_mul_f32 v[70:71], v[70:71], v[168:169]
	s_nop 0
	v_add_f32_e32 v64, v70, v71

.LBB0_737:
	s_or_b64 exec, exec, s[2:3]
	s_waitcnt lgkmcnt(0)
	s_nop 1
	v_mov_b32_dpp v71, v65 quad_perm:[1,0,3,2] row_mask:0xf bank_mask:0xf
	v_cmp_lt_i32_e32 vcc, 0, v96
	s_and_saveexec_b64 s[2:3], vcc
	s_xor_b64 s[2:3], exec, s[2:3]
	s_cbranch_execz .LBB0_741
	v_cmp_eq_u32_e32 vcc, 1, v96
	s_and_saveexec_b64 s[10:11], vcc
	s_cbranch_execz .LBB0_740
	v_mov_b32_e32 v70, v65
	s_waitcnt lgkmcnt(0)
	v_mul_f32_e32 v72, v71, v167
	v_pk_fma_f32 v[70:71], v[70:71], v[166:167], v[72:73] op_sel_hi:[1,1,0]
	s_nop 0
	v_mov_b32_e32 v65, v70

.LBB0_743:
	s_or_b64 exec, exec, s[2:3]
	s_waitcnt lgkmcnt(0)
	s_nop 1
	v_mov_b32_dpp v71, v62 quad_perm:[1,0,3,2] row_mask:0xf bank_mask:0xf
	v_cmp_lt_i32_e32 vcc, 0, v96
	s_and_saveexec_b64 s[2:3], vcc
	s_xor_b64 s[2:3], exec, s[2:3]
	s_cbranch_execz .LBB0_747
	v_cmp_eq_u32_e32 vcc, 1, v96
	s_and_saveexec_b64 s[10:11], vcc
	s_cbranch_execz .LBB0_746
	v_mov_b32_e32 v70, v62
	s_waitcnt lgkmcnt(0)
	v_pk_mul_f32 v[70:71], v[70:71], v[88:89]
	s_nop 0
	v_add_f32_e32 v62, v70, v71

.LBB0_749:
	s_or_b64 exec, exec, s[2:3]
	s_waitcnt lgkmcnt(0)
	s_nop 1
	v_mov_b32_dpp v71, v63 quad_perm:[1,0,3,2] row_mask:0xf bank_mask:0xf
	v_cmp_lt_i32_e32 vcc, 0, v96
	s_and_saveexec_b64 s[2:3], vcc
	s_xor_b64 s[2:3], exec, s[2:3]
	s_cbranch_execz .LBB0_755
	v_cmp_eq_u32_e32 vcc, 1, v96
	s_and_saveexec_b64 s[10:11], vcc
	s_cbranch_execz .LBB0_752
	v_mov_b32_e32 v70, v63
	s_waitcnt lgkmcnt(0)
	v_mul_f32_e32 v72, v71, v87
	v_pk_fma_f32 v[70:71], v[70:71], v[86:87], v[72:73] op_sel_hi:[1,1,0]
	s_nop 0
	v_mov_b32_e32 v63, v70

.LBB0_759:
	s_or_b64 exec, exec, s[2:3]
	v_lshlrev_b32_e32 v74, 16, v50
	ds_bpermute_b32 v76, v232, v98
	ds_bpermute_b32 v75, v232, v163
	ds_bpermute_b32 v72, v233, v98
	ds_bpermute_b32 v73, v233, v163
	ds_bpermute_b32 v70, v234, v98
	ds_bpermute_b32 v63, v234, v163
	ds_bpermute_b32 v68, v235, v98
	ds_bpermute_b32 v69, v235, v163
	ds_bpermute_b32 v66, v236, v98
	ds_bpermute_b32 v65, v236, v163
	ds_bpermute_b32 v60, v237, v98
	ds_bpermute_b32 v61, v237, v163
	ds_bpermute_b32 v58, v238, v98
	ds_bpermute_b32 v57, v238, v163
	ds_bpermute_b32 v54, v239, v98
	ds_bpermute_b32 v55, v239, v163
	s_nop 1
	v_mov_b32_dpp v77, v74 quad_perm:[1,0,3,2] row_mask:0xf bank_mask:0xf
	v_and_b32_e32 v1, 0xffff0000, v50
	v_cmp_lt_i32_e32 vcc, 0, v96
	s_and_saveexec_b64 s[2:3], vcc
	s_xor_b64 s[2:3], exec, s[2:3]
	s_cbranch_execz .LBB0_763
	v_cmp_eq_u32_e32 vcc, 1, v96
	s_and_saveexec_b64 s[10:11], vcc
	s_cbranch_execz .LBB0_762
	s_waitcnt lgkmcnt(0)
	v_pk_mul_f32 v[74:75], v[74:75], v[76:77]
	s_nop 0
	v_add_f32_e32 v74, v74, v75

.LBB0_765:
	s_or_b64 exec, exec, s[2:3]
	s_waitcnt lgkmcnt(13)
	s_nop 1
	v_mov_b32_dpp v75, v1 quad_perm:[1,0,3,2] row_mask:0xf bank_mask:0xf
	v_mov_b32_e32 v50, v74
	v_cmp_lt_i32_e32 vcc, 0, v96
	s_and_saveexec_b64 s[2:3], vcc
	s_xor_b64 s[2:3], exec, s[2:3]
	s_cbranch_execz .LBB0_769
	v_cmp_eq_u32_e32 vcc, 1, v96
	s_and_saveexec_b64 s[10:11], vcc
	s_cbranch_execz .LBB0_768
	v_mov_b32_e32 v76, v1
	s_waitcnt lgkmcnt(0)
	v_mov_b32_e32 v77, v73
	s_waitcnt lgkmcnt(0)
	v_mov_b32_e32 v73, v75
	v_mul_f32_e32 v56, v1, v72
	v_pk_fma_f32 v[72:73], v[76:77], v[72:73], v[56:57] op_sel_hi:[1,1,0]
	s_nop 0
	v_mov_b32_e32 v1, v73

.LBB0_771:
	s_or_b64 exec, exec, s[2:3]
	v_lshlrev_b32_e32 v62, 16, v51
	s_nop 1
	v_mov_b32_dpp v71, v62 quad_perm:[1,0,3,2] row_mask:0xf bank_mask:0xf
	v_and_b32_e32 v51, 0xffff0000, v51
	v_cmp_lt_i32_e32 vcc, 0, v96
	s_and_saveexec_b64 s[2:3], vcc
	s_xor_b64 s[2:3], exec, s[2:3]
	s_cbranch_execz .LBB0_775
	v_cmp_eq_u32_e32 vcc, 1, v96
	s_and_saveexec_b64 s[10:11], vcc
	s_cbranch_execz .LBB0_774
	s_waitcnt lgkmcnt(0)
	v_pk_mul_f32 v[62:63], v[70:71], v[62:63]
	s_nop 0
	v_add_f32_e32 v62, v62, v63

.LBB0_777:
	s_or_b64 exec, exec, s[2:3]
	s_waitcnt lgkmcnt(0)
	s_nop 1
	v_mov_b32_dpp v71, v51 quad_perm:[1,0,3,2] row_mask:0xf bank_mask:0xf
	v_cmp_lt_i32_e32 vcc, 0, v96
	s_and_saveexec_b64 s[2:3], vcc
	s_xor_b64 s[2:3], exec, s[2:3]
	s_cbranch_execz .LBB0_781
	v_cmp_eq_u32_e32 vcc, 1, v96
	s_and_saveexec_b64 s[10:11], vcc
	s_cbranch_execz .LBB0_780
	v_mov_b32_e32 v72, v51
	v_mov_b32_e32 v73, v69
	s_waitcnt lgkmcnt(0)
	v_mov_b32_e32 v69, v71
	v_mul_f32_e32 v56, v51, v68
	v_pk_fma_f32 v[68:69], v[72:73], v[68:69], v[56:57] op_sel_hi:[1,1,0]
	s_nop 0
	v_mov_b32_e32 v51, v69

.LBB0_783:
	s_or_b64 exec, exec, s[2:3]
	v_lshlrev_b32_e32 v64, 16, v52
	s_nop 1
	v_mov_b32_dpp v67, v64 quad_perm:[1,0,3,2] row_mask:0xf bank_mask:0xf
	v_and_b32_e32 v63, 0xffff0000, v52
	v_cmp_lt_i32_e32 vcc, 0, v96
	s_and_saveexec_b64 s[2:3], vcc
	s_xor_b64 s[2:3], exec, s[2:3]
	s_cbranch_execz .LBB0_787
	v_cmp_eq_u32_e32 vcc, 1, v96
	s_and_saveexec_b64 s[10:11], vcc
	s_cbranch_execz .LBB0_786
	s_waitcnt lgkmcnt(0)
	v_pk_mul_f32 v[64:65], v[66:67], v[64:65]
	s_nop 0
	v_add_f32_e32 v64, v64, v65

.LBB0_789:
	s_or_b64 exec, exec, s[2:3]
	s_waitcnt lgkmcnt(0)
	s_nop 1
	v_mov_b32_dpp v67, v63 quad_perm:[1,0,3,2] row_mask:0xf bank_mask:0xf
	v_cmp_lt_i32_e32 vcc, 0, v96
	s_and_saveexec_b64 s[2:3], vcc
	s_xor_b64 s[2:3], exec, s[2:3]
	s_cbranch_execz .LBB0_793
	v_cmp_eq_u32_e32 vcc, 1, v96
	s_and_saveexec_b64 s[10:11], vcc
	s_cbranch_execz .LBB0_792
	v_mov_b32_e32 v68, v63
	v_mov_b32_e32 v69, v61
	s_waitcnt lgkmcnt(0)
	v_mov_b32_e32 v61, v67
	v_mul_f32_e32 v52, v63, v60
	v_pk_fma_f32 v[60:61], v[68:69], v[60:61], v[52:53] op_sel_hi:[1,1,0]
	s_nop 0
	v_mov_b32_e32 v63, v61

.LBB0_795:
	s_or_b64 exec, exec, s[2:3]
	v_lshlrev_b32_e32 v56, 16, v53
	s_nop 1
	v_mov_b32_dpp v59, v56 quad_perm:[1,0,3,2] row_mask:0xf bank_mask:0xf
	v_and_b32_e32 v53, 0xffff0000, v53
	v_cmp_lt_i32_e32 vcc, 0, v96
	s_and_saveexec_b64 s[2:3], vcc
	s_xor_b64 s[2:3], exec, s[2:3]
	s_cbranch_execz .LBB0_799
	v_cmp_eq_u32_e32 vcc, 1, v96
	s_and_saveexec_b64 s[10:11], vcc
	s_cbranch_execz .LBB0_798
	s_waitcnt lgkmcnt(0)
	v_pk_mul_f32 v[56:57], v[58:59], v[56:57]
	s_nop 0
	v_add_f32_e32 v56, v56, v57

.LBB0_801:
	s_or_b64 exec, exec, s[2:3]
	s_waitcnt lgkmcnt(0)
	s_nop 1
	v_mov_b32_dpp v59, v53 quad_perm:[1,0,3,2] row_mask:0xf bank_mask:0xf
	v_cmp_lt_i32_e32 vcc, 0, v96
	s_and_saveexec_b64 s[2:3], vcc
	s_xor_b64 s[2:3], exec, s[2:3]
	s_cbranch_execz .LBB0_805
	v_cmp_eq_u32_e32 vcc, 1, v96
	s_and_saveexec_b64 s[10:11], vcc
	s_cbranch_execz .LBB0_804
	v_mov_b32_e32 v60, v53
	v_mov_b32_e32 v61, v55
	s_waitcnt lgkmcnt(0)
	v_mov_b32_e32 v55, v59
	v_mul_f32_e32 v52, v53, v54
	v_pk_fma_f32 v[52:53], v[60:61], v[54:55], v[52:53] op_sel_hi:[1,1,0]

.LBB0_807:
	s_or_b64 exec, exec, s[2:3]
	v_lshl_add_u64 v[54:55], s[88:89], 0, v[154:155]
	v_cvt_pk_bf16_f32 v50, v50, v1
	v_cvt_pk_bf16_f32 v51, v62, v51
	v_cvt_pk_bf16_f32 v52, v64, v63
	v_cvt_pk_bf16_f32 v53, v56, v53
	global_store_dwordx4 v[54:55], v[50:53], off
	global_load_dword v1, v[106:107], off
	v_and_or_b32 v56, v94, 15, v215
	v_mul_f32_e32 v50, v249, v249
	ds_bpermute_b32 v50, v211, v50
	v_ashrrev_i32_e32 v52, 4, v94
	s_waitcnt lgkmcnt(0)
	v_fmac_f32_e32 v50, v249, v249
	ds_bpermute_b32 v51, v212, v50
	s_waitcnt lgkmcnt(0)
	v_add_f32_e32 v50, v50, v51
	ds_bpermute_b32 v51, v213, v50
	s_waitcnt lgkmcnt(0)
	v_add_f32_e32 v50, v50, v51
	ds_bpermute_b32 v51, v210, v50
	s_waitcnt lgkmcnt(0)
	v_add_f32_e32 v50, v50, v51
	ds_bpermute_b32 v51, v209, v50
	s_waitcnt lgkmcnt(0)
	v_add_f32_e32 v53, v50, v51
	s_nop 1
	v_mov_b32_dpp v54, v53 quad_perm:[1,0,3,2] row_mask:0xf bank_mask:0xf
	ds_bpermute_b32 v50, v214, v98
	ds_bpermute_b32 v51, v214, v163
	v_lshlrev_b32_e32 v98, 4, v56
	v_mov_b32_e32 v163, v99
	s_waitcnt lgkmcnt(2)
	v_add_f32_e32 v53, v53, v54
	v_fmamk_f32 v53, v53, 0x3c800000, v95
	v_mul_f32_e32 v54, 0x4b800000, v53
	v_cmp_gt_f32_e32 vcc, s50, v53
	s_nop 1
	v_cndmask_b32_e32 v53, v53, v54, vcc
	v_rsq_f32_e32 v54, v53
	v_ashrrev_i32_e32 v53, 31, v52
	v_lshlrev_b64 v[52:53], 11, v[52:53]
	v_lshl_add_u64 v[52:53], v[100:101], 0, v[52:53]
	v_mul_f32_e32 v55, 0x45800000, v54
	v_cndmask_b32_e32 v54, v54, v55, vcc
	v_mul_f32_e32 v54, v249, v54
	v_lshl_add_u64 v[52:53], v[52:53], 0, v[98:99]
	s_waitcnt vmcnt(0)
	v_mul_f32_e32 v54, v1, v54
	ds_bpermute_b32 v55, v213, v54
	s_waitcnt lgkmcnt(0)
	v_pk_mul_f32 v[50:51], v[54:55], v[50:51]
	s_nop 0
	v_sub_f32_e32 v1, v50, v51
	v_add_f32_e32 v50, v51, v50
	v_cndmask_b32_e64 v50, v54, v50, s[0:1]
	v_cndmask_b32_e64 v1, v50, v1, s[6:7]
	v_cvt_pk_bf16_f32 v1, v1, s0
	v_lshl_add_u64 v[50:51], v[52:53], 0, v[162:163]
	global_store_short v[50:51], v1, off
	s_and_saveexec_b64 s[2:3], s[6:7]
	s_cbranch_execz .LBB0_809
	v_mul_f32_e32 v1, 0x3d3504f3, v248
	v_lshl_add_u64 v[50:51], s[88:89], 0, v[140:141]
	global_store_dword v[50:51], v1, off

.LBB0_1323:
	s_or_b64 exec, exec, s[18:19]
	s_waitcnt lgkmcnt(0)
	s_barrier
	ds_read_b128 v[2:5], v65 offset:52224
	v_add_u32_e32 v18, v25, v57
	ds_read_b128 v[6:9], v18 offset:17408
	ds_read_b128 v[10:13], v65 offset:52288
	ds_read_b128 v[14:17], v18 offset:17472
	ds_read_b128 v[38:41], v65 offset:56576
	ds_read_b128 v[42:45], v65 offset:56640
	ds_read_b128 v[74:77], v65 offset:60928
	ds_read_b128 v[78:81], v65 offset:60992
	ds_read_b128 v[86:89], v65 offset:65280
	ds_read_b128 v[90:93], v65 offset:65344
	ds_read_b128 v[94:97], v18 offset:21760
	ds_read_b128 v[98:101], v18 offset:21824
	s_waitcnt lgkmcnt(10)
	v_mfma_f32_16x16x32_bf16 v[34:37], v[2:5], v[6:9], 0
	s_lshl_b32 s8, s16, 10
	s_lshl_b32 s9, s44, 4
	s_or_b32 s44, s9, s8
	s_waitcnt lgkmcnt(7)
	v_mfma_f32_16x16x32_bf16 v[46:49], v[38:41], v[6:9], 0
	v_mov_b32_e32 v29, v19
	s_lshl_b32 s25, s45, 3
	s_lshl_b32 s24, s45, 9
	s_waitcnt lgkmcnt(1)
	v_mfma_f32_16x16x32_bf16 v[2:5], v[2:5], v[94:97], 0
	s_mov_b32 s45, 0
	v_mfma_f32_16x16x32_bf16 v[38:41], v[38:41], v[94:97], 0
	v_mfma_f32_16x16x32_bf16 v[34:37], v[10:13], v[14:17], v[34:37]
	s_waitcnt lgkmcnt(0)
	v_mfma_f32_16x16x32_bf16 v[2:5], v[10:13], v[98:101], v[2:5]
	v_mfma_f32_16x16x32_bf16 v[10:13], v[42:45], v[98:101], v[38:41]
	s_nop 3
	ds_read_b128 v[38:41], v65 offset:52352
	v_mfma_f32_16x16x32_bf16 v[82:85], v[74:77], v[6:9], 0
	v_mfma_f32_16x16x32_bf16 v[6:9], v[86:89], v[6:9], 0
	v_mfma_f32_16x16x32_bf16 v[74:77], v[74:77], v[94:97], 0
	v_mfma_f32_16x16x32_bf16 v[86:89], v[86:89], v[94:97], 0
	v_mfma_f32_16x16x32_bf16 v[46:49], v[42:45], v[14:17], v[46:49]
	v_mfma_f32_16x16x32_bf16 v[82:85], v[78:81], v[14:17], v[82:85]
	v_mfma_f32_16x16x32_bf16 v[6:9], v[90:93], v[14:17], v[6:9]
	v_mfma_f32_16x16x32_bf16 v[14:17], v[78:81], v[98:101], v[74:77]
	v_mfma_f32_16x16x32_bf16 v[42:45], v[90:93], v[98:101], v[86:89]
	s_nop 1
	ds_read_b128 v[74:77], v18 offset:17536
	ds_read_b128 v[78:81], v18 offset:17600
	ds_read_b128 v[86:89], v65 offset:52416
	ds_read_b128 v[90:93], v65 offset:56704
	ds_read_b128 v[94:97], v65 offset:56768
	ds_read_b128 v[98:101], v65 offset:61056
	ds_read_b128 v[102:105], v65 offset:61120
	ds_read_b128 v[106:109], v65 offset:65408
	ds_read_b128 v[110:113], v65 offset:65472
	s_waitcnt lgkmcnt(8)
	v_mfma_f32_16x16x32_bf16 v[34:37], v[38:41], v[74:77], v[34:37]
	s_waitcnt lgkmcnt(5)
	v_mfma_f32_16x16x32_bf16 v[46:49], v[90:93], v[74:77], v[46:49]
	s_waitcnt lgkmcnt(3)
	v_mfma_f32_16x16x32_bf16 v[82:85], v[98:101], v[74:77], v[82:85]
	s_waitcnt lgkmcnt(1)
	v_mfma_f32_16x16x32_bf16 v[6:9], v[106:109], v[74:77], v[6:9]
	ds_read_b128 v[74:77], v18 offset:21888
	ds_read_b128 v[114:117], v18 offset:21952
	v_mfma_f32_16x16x32_bf16 v[34:37], v[86:89], v[78:81], v[34:37]
	s_waitcnt lgkmcnt(1)
	v_mfma_f32_16x16x32_bf16 v[2:5], v[38:41], v[74:77], v[2:5]
	v_mfma_f32_16x16x32_bf16 v[38:41], v[106:109], v[74:77], v[42:45]
	v_mfma_f32_16x16x32_bf16 v[42:45], v[94:97], v[78:81], v[46:49]
	s_nop 3
	v_cvt_pk_bf16_f32 v46, v34, v35
	v_cvt_pk_bf16_f32 v47, v36, v37
	v_mfma_f32_16x16x32_bf16 v[34:37], v[102:105], v[78:81], v[82:85]
	s_nop 0
	v_cvt_pk_bf16_f32 v42, v42, v43
	v_cvt_pk_bf16_f32 v43, v44, v45
	ds_write2_b64 v66, v[46:47], v[42:43] offset1:4
	v_mfma_f32_16x16x32_bf16 v[6:9], v[110:113], v[78:81], v[6:9]
	v_mfma_f32_16x16x32_bf16 v[10:13], v[90:93], v[74:77], v[10:13]
	s_nop 1
	v_cvt_pk_bf16_f32 v34, v34, v35
	v_cvt_pk_bf16_f32 v35, v36, v37
	s_nop 2
	v_cvt_pk_bf16_f32 v6, v6, v7
	s_waitcnt lgkmcnt(1)
	v_mfma_f32_16x16x32_bf16 v[2:5], v[86:89], v[114:117], v[2:5]
	v_cvt_pk_bf16_f32 v7, v8, v9
	ds_write2_b64 v66, v[34:35], v[6:7] offset0:8 offset1:12
	v_mfma_f32_16x16x32_bf16 v[14:17], v[98:101], v[74:77], v[14:17]
	s_nop 4
	v_cvt_pk_bf16_f32 v6, v2, v3
	v_cvt_pk_bf16_f32 v7, v4, v5
	v_mfma_f32_16x16x32_bf16 v[2:5], v[94:97], v[114:117], v[10:13]
	s_nop 2
	v_add_u32_e32 v10, 0x1000, v66
	s_nop 3
	v_cvt_pk_bf16_f32 v8, v2, v3
	v_cvt_pk_bf16_f32 v9, v4, v5
	v_mfma_f32_16x16x32_bf16 v[2:5], v[102:105], v[114:117], v[14:17]
	ds_write2_b64 v10, v[6:7], v[8:9] offset0:32 offset1:36
	s_nop 6
	v_cvt_pk_bf16_f32 v6, v2, v3
	v_cvt_pk_bf16_f32 v7, v4, v5
	v_mfma_f32_16x16x32_bf16 v[2:5], v[110:113], v[114:117], v[38:41]
	s_nop 7
	v_cvt_pk_bf16_f32 v2, v2, v3
	v_cvt_pk_bf16_f32 v3, v4, v5
	ds_write2_b64 v10, v[6:7], v[2:3] offset0:40 offset1:44
	v_and_b32_e32 v3, 64, v71
	v_xor_b32_e32 v2, 1, v71
	v_add_u32_e32 v3, 64, v3
	v_cmp_lt_i32_e64 s[8:9], v2, v3
	v_or_b32_e32 v4, s43, v56
	s_waitcnt lgkmcnt(0)
	v_cndmask_b32_e64 v2, v71, v2, s[8:9]
	v_lshlrev_b32_e32 v74, 2, v2
	v_xor_b32_e32 v2, 2, v71
	v_cmp_lt_i32_e64 s[8:9], v2, v3
	s_barrier
	s_nop 0
	v_cndmask_b32_e64 v2, v71, v2, s[8:9]
	v_lshlrev_b32_e32 v75, 2, v2
	v_mov_b64_e32 v[2:3], s[12:13]
	v_mad_i64_i32 v[34:35], s[8:9], v4, s34, v[2:3]
	v_add_u32_e32 v2, s43, v60
	v_ashrrev_i32_e32 v3, 31, v2
	v_mov_b64_e32 v[4:5], s[88:89]
	v_mad_i64_i32 v[36:37], s[8:9], v2, s34, 0
	v_mad_i64_i32 v[6:7], s[8:9], v2, s39, v[4:5]
	v_lshlrev_b64 v[2:3], 12, v[2:3]
	v_lshl_add_u64 v[40:41], v[26:27], 0, v[2:3]
	v_add_u32_e32 v2, s43, v63
	v_ashrrev_i32_e32 v3, 31, v2
	v_mad_i64_i32 v[4:5], s[8:9], v2, s39, v[4:5]
	v_lshl_add_u64 v[6:7], v[6:7], 0, v[28:29]
	v_mad_i64_i32 v[42:43], s[8:9], v2, s34, 0
	v_lshl_add_u64 v[4:5], v[4:5], 0, v[28:29]
	v_lshlrev_b64 v[2:3], 12, v[2:3]
	v_lshl_add_u64 v[38:39], v[6:7], 0, s[2:3]
	v_lshl_add_u64 v[44:45], v[4:5], 0, s[2:3]
	v_lshl_add_u64 v[46:47], v[26:27], 0, v[2:3]
	s_lshl_b32 s20, s24, 1
	s_mov_b32 s21, 0
	v_ashrrev_i32_e32 v170, 4, v1
	v_and_b32_e32 v170, -8, v170
	v_ashrrev_i32_e32 v171, 31, v170
	v_lshl_add_u64 v[168:169], v[34:35], 0, s[20:21]
	v_lshl_add_u64 v[168:169], v[170:171], 1, v[168:169]
	global_load_dwordx4 v[160:163], v[168:169], off
	global_load_dwordx4 v[164:167], v[168:169], off offset:64
	s_lshl_b32 s20, s24, 1
	s_mov_b32 s21, 0
	v_lshl_add_u64 v[180:181], v[22:23], 0, s[20:21]
	v_lshl_add_u64 v[180:181], v[180:181], 0, v[42:43]
	global_load_dwordx4 v[172:175], v[180:181], off
	v_lshl_add_u64 v[180:181], v[44:45], 0, s[20:21]
	global_load_dwordx4 v[176:179], v[180:181], off
	s_branch .LBB0_1325

.LBB0_1344:
	s_or_b64 exec, exec, s[18:19]
	s_lshl_b32 s22, s45, 6
	s_add_i32 s22, s22, s24
	s_and_saveexec_b64 s[18:19], s[0:1]
	s_cbranch_execz .LBB0_1347
	v_lshl_add_u32 v2, s45, 2, v58
	ds_read_b32 v4, v2 offset:4096
	s_waitcnt vmcnt(0) lgkmcnt(0)
	v_mov_b32_e32 v5, v1
	v_ashrrev_i32_e32 v12, 4, v5
	v_and_b32_e32 v10, -8, v12
	v_or_b32_e32 v12, 7, v12
	v_mad_u64_u32 v[10:11], s[8:9], v10, s28, v[24:25]
	v_mad_u64_u32 v[12:13], s[8:9], v12, s28, v[24:25]
	v_lshlrev_b32_e32 v11, 16, v160
	v_and_b32_e32 v6, 0xffff0000, v160
	v_lshlrev_b32_e32 v13, 16, v161
	v_and_b32_e32 v7, 0xffff0000, v161
	v_lshlrev_b32_e32 v14, 16, v162
	v_and_b32_e32 v8, 0xffff0000, v162
	v_lshlrev_b32_e32 v15, 16, v163
	v_and_b32_e32 v9, 0xffff0000, v163
	v_mul_f32_e32 v11, v4, v11
	v_mul_f32_e32 v6, v4, v6
	v_mul_f32_e32 v13, v4, v13
	v_mul_f32_e32 v7, v4, v7
	v_mul_f32_e32 v14, v4, v14
	v_mul_f32_e32 v8, v4, v8
	v_mul_f32_e32 v15, v4, v15
	v_mul_f32_e32 v9, v4, v9
	v_cvt_pk_bf16_f32 v11, v11, s0
	v_cvt_pk_bf16_f32 v6, v6, s0
	v_cvt_pk_bf16_f32 v13, v13, s0
	v_cvt_pk_bf16_f32 v7, v7, s0
	v_cvt_pk_bf16_f32 v14, v14, s0
	v_cvt_pk_bf16_f32 v8, v8, s0
	v_cvt_pk_bf16_f32 v15, v15, s0
	v_cvt_pk_bf16_f32 v9, v9, s0
	ds_write_b16 v10, v11
	ds_write_b16 v10, v6 offset:272
	ds_write_b16 v10, v13 offset:544
	ds_write_b16 v10, v7 offset:816
	ds_write_b16 v10, v14 offset:1088
	ds_write_b16 v10, v8 offset:1360
	ds_write_b16 v10, v15 offset:1632
	ds_write_b16 v12, v9
	v_add_u32_e32 v5, 512, v1
	v_ashrrev_i32_e32 v12, 4, v5
	v_and_b32_e32 v10, -8, v12
	v_or_b32_e32 v12, 7, v12
	v_mad_u64_u32 v[10:11], s[8:9], v10, s28, v[24:25]
	v_mad_u64_u32 v[12:13], s[8:9], v12, s28, v[24:25]
	v_lshlrev_b32_e32 v11, 16, v164
	v_and_b32_e32 v6, 0xffff0000, v164
	v_lshlrev_b32_e32 v13, 16, v165
	v_and_b32_e32 v7, 0xffff0000, v165
	v_lshlrev_b32_e32 v14, 16, v166
	v_and_b32_e32 v8, 0xffff0000, v166
	v_lshlrev_b32_e32 v15, 16, v167
	v_and_b32_e32 v9, 0xffff0000, v167
	v_mul_f32_e32 v11, v4, v11
	v_mul_f32_e32 v6, v4, v6
	v_mul_f32_e32 v13, v4, v13
	v_mul_f32_e32 v7, v4, v7
	v_mul_f32_e32 v14, v4, v14
	v_mul_f32_e32 v8, v4, v8
	v_mul_f32_e32 v15, v4, v15
	v_mul_f32_e32 v9, v4, v9
	v_cvt_pk_bf16_f32 v11, v11, s0
	v_cvt_pk_bf16_f32 v6, v6, s0
	v_cvt_pk_bf16_f32 v13, v13, s0
	v_cvt_pk_bf16_f32 v7, v7, s0
	v_cvt_pk_bf16_f32 v14, v14, s0
	v_cvt_pk_bf16_f32 v8, v8, s0
	v_cvt_pk_bf16_f32 v15, v15, s0
	v_cvt_pk_bf16_f32 v9, v9, s0
	ds_write_b16 v10, v11
	ds_write_b16 v10, v6 offset:272
	ds_write_b16 v10, v13 offset:544
	ds_write_b16 v10, v7 offset:816
	ds_write_b16 v10, v14 offset:1088
	ds_write_b16 v10, v8 offset:1360
	ds_write_b16 v10, v15 offset:1632
	ds_write_b16 v12, v9
	s_cmp_lt_u32 s45, 7
	s_cbranch_scc0 .Lxt_nopf
	s_lshl_b32 s20, s22, 1
	s_add_i32 s20, s20, 0x80
	s_mov_b32 s21, 0
	v_ashrrev_i32_e32 v170, 4, v1
	v_and_b32_e32 v170, -8, v170
	v_ashrrev_i32_e32 v171, 31, v170
	v_lshl_add_u64 v[168:169], v[34:35], 0, s[20:21]
	v_lshl_add_u64 v[168:169], v[170:171], 1, v[168:169]
	global_load_dwordx4 v[160:163], v[168:169], off
	global_load_dwordx4 v[164:167], v[168:169], off offset:64
.Lxt_nopf:
.LBB0_1347:
	s_or_b64 exec, exec, s[18:19]
	s_waitcnt lgkmcnt(0)
	s_barrier
	ds_read_b128 v[2:5], v67
	ds_read_b128 v[6:9], v18 offset:52224
	ds_read_b128 v[10:13], v18 offset:52288
	ds_read_b128 v[14:17], v67 offset:64
	ds_read_b128 v[76:79], v67 offset:4352
	ds_read_b128 v[80:83], v67 offset:4416
	ds_read_b128 v[84:87], v18 offset:56576
	ds_read_b128 v[88:91], v18 offset:56640
	s_add_i32 s16, s45, s25
	s_add_i32 s8, s44, s16
	s_waitcnt lgkmcnt(6)
	v_mfma_f32_16x16x32_bf16 v[48:51], v[2:5], v[6:9], 0
	s_ashr_i32 s9, s8, 31
	s_lshl_b64 s[8:9], s[8:9], 14
	v_lshl_add_u64 v[92:93], v[20:21], 0, s[8:9]
	s_waitcnt lgkmcnt(3)
	v_mfma_f32_16x16x32_bf16 v[6:9], v[76:79], v[6:9], 0
	v_mov_b32_e32 v31, v19
	v_mov_b32_e32 v33, v19
	v_lshl_add_u64 v[140:141], v[92:93], 0, v[30:31]
	s_waitcnt lgkmcnt(1)
	v_mfma_f32_16x16x32_bf16 v[2:5], v[2:5], v[84:87], 0
	v_lshl_add_u64 v[152:153], v[92:93], 0, v[32:33]
	s_lshl_b64 s[8:9], s[16:17], 2
	s_add_u32 s8, s56, s8
	v_mfma_f32_16x16x32_bf16 v[76:79], v[76:79], v[84:87], 0
	global_load_dwordx4 v[84:87], v[140:141], off
	s_addc_u32 s9, s57, s9
	s_lshl_b32 s16, s22, 1
	v_mfma_f32_16x16x32_bf16 v[48:51], v[14:17], v[10:13], v[48:51]
	v_add_u32_e32 v29, s46, v59
	v_mfma_f32_16x16x32_bf16 v[6:9], v[80:83], v[10:13], v[6:9]
	global_load_dwordx4 v[10:13], v[152:153], off
	s_waitcnt lgkmcnt(0)
	v_mfma_f32_16x16x32_bf16 v[2:5], v[14:17], v[88:91], v[2:5]
	ds_read_b128 v[14:17], v67 offset:128
	ds_read_b128 v[92:95], v18 offset:52352
	v_mfma_f32_16x16x32_bf16 v[76:79], v[80:83], v[88:91], v[76:79]
	ds_read_b128 v[80:83], v67 offset:4480
	ds_read_b128 v[88:91], v18 offset:52416
	ds_read_b128 v[96:99], v67 offset:192
	global_load_dwordx4 v[100:103], v[140:141], off offset:64
	global_load_dwordx4 v[108:111], v[152:153], off offset:64
	s_waitcnt lgkmcnt(3)
	v_mfma_f32_16x16x32_bf16 v[48:51], v[14:17], v[92:95], v[48:51]
	ds_read_b128 v[104:107], v67 offset:4544
	s_waitcnt lgkmcnt(3)
	v_mfma_f32_16x16x32_bf16 v[6:9], v[80:83], v[92:95], v[6:9]
	ds_read_b128 v[92:95], v18 offset:56704
	ds_read_b128 v[112:115], v18 offset:56768
	s_waitcnt lgkmcnt(1)
	v_mfma_f32_16x16x32_bf16 v[2:5], v[14:17], v[92:95], v[2:5]
	ds_read_b128 v[14:17], v18 offset:17408
	ds_read_b128 v[116:119], v18 offset:17472
	global_load_dwordx4 v[120:123], v[140:141], off offset:128
	ds_read_b128 v[128:131], v18 offset:21760
	ds_read_b128 v[132:135], v18 offset:21824
	global_load_dwordx4 v[136:139], v[152:153], off offset:128
	v_mfma_f32_16x16x32_bf16 v[124:127], v[96:99], v[88:91], v[48:51]
	global_load_dwordx4 v[140:143], v[140:141], off offset:192
	s_nop 1
	v_lshl_add_u64 v[50:51], v[22:23], 0, s[16:17]
	v_lshl_add_u64 v[144:145], v[50:51], 0, v[36:37]
	v_lshl_add_u64 v[48:49], v[38:39], 0, s[16:17]
	global_load_dwordx4 v[144:147], v[144:145], off
	s_nop 0
	global_load_dwordx4 v[148:151], v[48:49], off
	v_mfma_f32_16x16x32_bf16 v[6:9], v[104:107], v[88:91], v[6:9]
	global_load_dwordx4 v[152:155], v[152:153], off offset:192
	ds_read_b32 v29, v29
	global_load_dword v48, v19, s[8:9]
	s_waitcnt lgkmcnt(5)
	v_mfma_f32_16x16x32_bf16 v[2:5], v[96:99], v[112:115], v[2:5]
	s_waitcnt lgkmcnt(0)
	v_mul_f32_e32 v31, 0x3fb8aa3b, v29
	v_fma_f32 v33, v29, s35, -v31
	v_rndne_f32_e32 v49, v31
	v_fmac_f32_e32 v33, 0x32a5705f, v29
	v_sub_f32_e32 v31, v31, v49
	v_add_f32_e32 v31, v31, v33
	v_cvt_i32_f32_e32 v49, v49
	v_exp_f32_e32 v31, v31
	v_cmp_ngt_f32_e64 s[8:9], s36, v29
	s_waitcnt vmcnt(10)
	v_mfma_f32_16x16x32_bf16 v[88:91], v[84:87], v[14:17], 0
	v_ldexp_f32 v31, v31, v49
	v_cndmask_b32_e64 v31, 0, v31, s[8:9]
	v_cmp_nlt_f32_e64 s[8:9], s37, v29
	s_waitcnt vmcnt(9)
	v_mfma_f32_16x16x32_bf16 v[14:17], v[10:13], v[14:17], 0
	v_mfma_f32_16x16x32_bf16 v[84:87], v[84:87], v[128:131], 0
	v_mfma_f32_16x16x32_bf16 v[10:13], v[10:13], v[128:131], 0
	s_waitcnt vmcnt(8)
	v_mfma_f32_16x16x32_bf16 v[88:91], v[100:103], v[116:119], v[88:91]
	s_waitcnt vmcnt(7)
	v_mfma_f32_16x16x32_bf16 v[14:17], v[108:111], v[116:119], v[14:17]
	ds_read_b128 v[116:119], v18 offset:17536
	ds_read_b128 v[128:131], v18 offset:17600
	s_waitcnt vmcnt(6) lgkmcnt(1)
	v_mfma_f32_16x16x32_bf16 v[88:91], v[120:123], v[116:119], v[88:91]
	s_waitcnt vmcnt(5)
	v_mfma_f32_16x16x32_bf16 v[14:17], v[136:139], v[116:119], v[14:17]
	v_cndmask_b32_e64 v116, v70, v31, s[8:9]
	s_waitcnt vmcnt(3)
	v_lshlrev_b32_e32 v118, 16, v144
	v_and_b32_e32 v119, 0xffff0000, v144
	v_mfma_f32_16x16x32_bf16 v[84:87], v[100:103], v[132:135], v[84:87]
	v_mfma_f32_16x16x32_bf16 v[10:13], v[108:111], v[132:135], v[10:13]
	ds_read_b128 v[100:103], v18 offset:21888
	ds_read_b128 v[108:111], v18 offset:21952
	s_waitcnt lgkmcnt(2)
	v_mfma_f32_16x16x32_bf16 v[88:91], v[140:143], v[128:131], v[88:91]
	s_waitcnt vmcnt(1)
	v_mfma_f32_16x16x32_bf16 v[14:17], v[152:155], v[128:131], v[14:17]
	s_waitcnt lgkmcnt(1)
	v_mfma_f32_16x16x32_bf16 v[84:87], v[120:123], v[100:103], v[84:87]
	v_lshlrev_b32_e32 v120, 16, v148
	v_and_b32_e32 v121, 0xffff0000, v148
	s_nop 1
	v_pk_fma_f32 v[88:89], v[88:89], v[116:117], v[124:125] op_sel_hi:[1,0,1]
	v_pk_fma_f32 v[90:91], v[90:91], v[116:117], v[126:127] op_sel_hi:[1,0,1]
	v_pk_fma_f32 v[6:7], v[14:15], v[116:117], v[6:7] op_sel_hi:[1,0,1]
	v_mul_f32_e32 v29, 0xbfb8aa3b, v120
	v_pk_fma_f32 v[8:9], v[16:17], v[116:117], v[8:9] op_sel_hi:[1,0,1]
	ds_write_b128 v72, v[88:91]
	ds_write_b128 v72, v[6:9] offset:64
	v_mul_f32_e32 v6, 0xbfb8aa3b, v121
	v_exp_f32_e32 v29, v29
	v_exp_f32_e32 v6, v6
	v_mfma_f32_16x16x32_bf16 v[14:17], v[80:83], v[92:95], v[76:79]
	s_nop 2
	ds_read_b128 v[76:79], v73
	ds_read_b128 v[80:83], v73 offset:16
	v_add_f32_e32 v7, 1.0, v29
	v_add_f32_e32 v6, 1.0, v6
	v_mfma_f32_16x16x32_bf16 v[88:91], v[136:139], v[100:103], v[10:13]
	v_lshlrev_b32_e32 v92, 16, v146
	v_and_b32_e32 v93, 0xffff0000, v146
	s_waitcnt vmcnt(0) lgkmcnt(0)
	v_pk_fma_f32 v[80:81], v[48:49], v[92:93], v[80:81] op_sel_hi:[0,1,1]
	v_rcp_f32_e32 v10, v7
	v_rcp_f32_e32 v11, v6
	v_pk_fma_f32 v[12:13], v[48:49], v[118:119], v[76:77] op_sel_hi:[0,1,1]
	v_mfma_f32_16x16x32_bf16 v[6:9], v[140:143], v[108:111], v[84:87]
	v_lshlrev_b32_e32 v94, 16, v147
	v_pk_mul_f32 v[10:11], v[10:11], v[120:121]
	v_and_b32_e32 v95, 0xffff0000, v147
	v_pk_mul_f32 v[76:77], v[12:13], v[10:11]
	v_mfma_f32_16x16x32_bf16 v[10:13], v[104:107], v[112:115], v[14:17]
	v_lshlrev_b32_e32 v86, 16, v145
	v_and_b32_e32 v87, 0xffff0000, v145
	v_pk_fma_f32 v[78:79], v[48:49], v[86:87], v[78:79] op_sel_hi:[0,1,1]
	v_lshlrev_b32_e32 v14, 16, v149
	v_and_b32_e32 v15, 0xffff0000, v149
	v_mul_f32_e32 v16, 0xbfb8aa3b, v14
	v_exp_f32_e32 v29, v16
	v_mul_f32_e32 v16, 0xbfb8aa3b, v15
	v_exp_f32_e32 v31, v16
	v_pk_mul_f32 v[16:17], v[76:77], v[76:77]
	v_add_f32_e32 v29, 1.0, v29
	v_rcp_f32_e32 v84, v29
	v_add_f32_e32 v29, 1.0, v31
	v_rcp_f32_e32 v85, v29
	v_add_f32_e32 v16, v16, v17
	v_pk_fma_f32 v[82:83], v[48:49], v[94:95], v[82:83] op_sel_hi:[0,1,1]
	v_cvt_pk_bf16_f32 v76, v76, v77
	v_pk_mul_f32 v[14:15], v[84:85], v[14:15]
	s_nop 0
	v_pk_mul_f32 v[78:79], v[78:79], v[14:15]
	v_lshlrev_b32_e32 v14, 16, v150
	v_and_b32_e32 v15, 0xffff0000, v150
	v_mul_f32_e32 v29, 0xbfb8aa3b, v14
	v_exp_f32_e32 v29, v29
	v_mul_f32_e32 v31, 0xbfb8aa3b, v15
	v_exp_f32_e32 v31, v31
	v_pk_mul_f32 v[84:85], v[78:79], v[78:79]
	v_add_f32_e32 v29, 1.0, v29
	v_rcp_f32_e32 v86, v29
	v_add_f32_e32 v29, 1.0, v31
	v_rcp_f32_e32 v87, v29
	v_add_f32_e32 v16, v84, v16
	v_add_f32_e32 v16, v85, v16
	v_lshl_add_u64 v[84:85], v[40:41], 0, s[16:17]
	v_pk_mul_f32 v[14:15], v[86:87], v[14:15]
	v_cvt_pk_bf16_f32 v77, v78, v79
	v_pk_mul_f32 v[80:81], v[80:81], v[14:15]
	v_lshlrev_b32_e32 v14, 16, v151
	v_and_b32_e32 v15, 0xffff0000, v151
	v_mul_f32_e32 v29, 0xbfb8aa3b, v14
	v_exp_f32_e32 v29, v29
	v_mul_f32_e32 v31, 0xbfb8aa3b, v15
	v_exp_f32_e32 v31, v31
	v_pk_mul_f32 v[86:87], v[80:81], v[80:81]
	v_add_f32_e32 v29, 1.0, v29
	v_rcp_f32_e32 v92, v29
	v_add_f32_e32 v29, 1.0, v31
	v_rcp_f32_e32 v93, v29
	v_add_f32_e32 v16, v86, v16
	v_add_f32_e32 v16, v87, v16
	v_lshl_add_u32 v29, s45, 3, v52
	v_pk_mul_f32 v[14:15], v[92:93], v[14:15]
	v_cvt_pk_bf16_f32 v78, v80, v81
	v_pk_mul_f32 v[82:83], v[82:83], v[14:15]
	s_nop 0
	v_pk_mul_f32 v[14:15], v[82:83], v[82:83]
	v_cvt_pk_bf16_f32 v79, v82, v83
	v_add_f32_e32 v14, v14, v16
	v_add_f32_e32 v31, v15, v14
	ds_bpermute_b32 v33, v74, v31
	v_mfma_f32_16x16x32_bf16 v[14:17], v[152:155], v[108:111], v[88:91]
	global_store_dwordx4 v[84:85], v[76:79], off offset:2048
	s_waitcnt lgkmcnt(0)
	v_add_f32_e32 v31, v31, v33
	ds_bpermute_b32 v33, v75, v31
	s_and_saveexec_b64 s[8:9], s[4:5]
	s_cbranch_execz .LBB0_1349
	s_waitcnt lgkmcnt(0)
	v_add_f32_e32 v31, v31, v33
	v_add_u32_e32 v33, v29, v61
	ds_write_b32 v33, v31 offset:8192
.LBB0_1349:
	s_or_b64 exec, exec, s[8:9]
	v_lshl_add_u64 v[50:51], v[50:51], 0, v[42:43]
	v_mov_b64_e32 v[76:77], v[172:173]
	v_mov_b64_e32 v[78:79], v[174:175]
	global_load_dwordx4 v[172:175], v[50:51], off offset:128
	v_lshl_add_u64 v[50:51], v[44:45], 0, s[16:17]
	v_mov_b64_e32 v[80:81], v[176:177]
	v_mov_b64_e32 v[82:83], v[178:179]
	global_load_dwordx4 v[176:179], v[50:51], off offset:128
	v_add_u32_e32 v31, s46, v62
	ds_read_b32 v31, v31
	s_waitcnt lgkmcnt(0)
	v_mul_f32_e32 v33, 0x3fb8aa3b, v31
	v_fma_f32 v49, v31, s35, -v33
	v_rndne_f32_e32 v50, v33
	v_fmac_f32_e32 v49, 0x32a5705f, v31
	v_sub_f32_e32 v33, v33, v50
	v_add_f32_e32 v33, v33, v49
	v_cvt_i32_f32_e32 v50, v50
	v_exp_f32_e32 v33, v33
	v_cmp_ngt_f32_e64 s[8:9], s36, v31
	v_mov_b32_e32 v49, v48
	v_ldexp_f32 v33, v33, v50
	v_cndmask_b32_e64 v33, 0, v33, s[8:9]
	v_cmp_nlt_f32_e64 s[8:9], s37, v31
	s_nop 1
	v_cndmask_b32_e64 v50, v70, v33, s[8:9]
	v_pk_fma_f32 v[4:5], v[8:9], v[50:51], v[4:5] op_sel_hi:[1,0,1]
	v_pk_fma_f32 v[2:3], v[6:7], v[50:51], v[2:3] op_sel_hi:[1,0,1]
	v_pk_fma_f32 v[8:9], v[16:17], v[50:51], v[12:13] op_sel_hi:[1,0,1]
	v_pk_fma_f32 v[6:7], v[14:15], v[50:51], v[10:11] op_sel_hi:[1,0,1]
	ds_write_b128 v72, v[2:5]
	ds_write_b128 v72, v[6:9] offset:64
	ds_read_b128 v[2:5], v73
	ds_read_b128 v[6:9], v73 offset:16
	v_lshlrev_b32_e32 v10, 16, v76
	v_and_b32_e32 v11, 0xffff0000, v76
	v_lshlrev_b32_e32 v12, 16, v80
	v_and_b32_e32 v13, 0xffff0000, v80
	v_lshlrev_b32_e32 v14, 16, v77
	v_and_b32_e32 v15, 0xffff0000, v77
	v_lshlrev_b32_e32 v16, 16, v81
	v_and_b32_e32 v17, 0xffff0000, v81
	v_mul_f32_e32 v31, 0xbfb8aa3b, v12
	s_waitcnt lgkmcnt(1)
	v_pk_fma_f32 v[2:3], v[48:49], v[10:11], v[2:3]
	v_mul_f32_e32 v10, 0xbfb8aa3b, v13
	v_lshlrev_b32_e32 v76, 16, v82
	v_mul_f32_e32 v11, 0xbfb8aa3b, v16
	v_pk_fma_f32 v[4:5], v[48:49], v[14:15], v[4:5]
	v_mul_f32_e32 v14, 0xbfb8aa3b, v17
	v_exp_f32_e32 v31, v31
	v_exp_f32_e32 v10, v10
	v_and_b32_e32 v77, 0xffff0000, v82
	v_mul_f32_e32 v15, 0xbfb8aa3b, v76
	v_exp_f32_e32 v11, v11
	v_exp_f32_e32 v14, v14
	v_lshlrev_b32_e32 v50, 16, v78
	v_and_b32_e32 v51, 0xffff0000, v78
	v_lshlrev_b32_e32 v78, 16, v79
	v_and_b32_e32 v79, 0xffff0000, v79
	v_lshlrev_b32_e32 v80, 16, v83
	v_and_b32_e32 v81, 0xffff0000, v83
	v_mul_f32_e32 v33, 0xbfb8aa3b, v77
	v_exp_f32_e32 v15, v15
	s_waitcnt lgkmcnt(0)
	v_pk_fma_f32 v[6:7], v[48:49], v[50:51], v[6:7]
	v_mul_f32_e32 v50, 0xbfb8aa3b, v80
	v_pk_fma_f32 v[8:9], v[48:49], v[78:79], v[8:9]
	v_mul_f32_e32 v48, 0xbfb8aa3b, v81
	v_exp_f32_e32 v33, v33
	v_exp_f32_e32 v49, v50
	v_exp_f32_e32 v48, v48
	v_add_f32_e32 v31, 1.0, v31
	v_add_f32_e32 v50, 1.0, v10
	v_add_f32_e32 v51, 1.0, v11
	v_add_f32_e32 v78, 1.0, v14
	v_rcp_f32_e32 v10, v31
	v_rcp_f32_e32 v11, v50
	v_add_f32_e32 v79, 1.0, v15
	v_rcp_f32_e32 v14, v51
	v_rcp_f32_e32 v15, v78
	v_add_f32_e32 v33, 1.0, v33
	v_add_f32_e32 v82, 1.0, v49
	v_add_f32_e32 v83, 1.0, v48
	v_rcp_f32_e32 v48, v79
	v_rcp_f32_e32 v49, v33
	v_pk_mul_f32 v[10:11], v[10:11], v[12:13]
	v_rcp_f32_e32 v50, v82
	v_rcp_f32_e32 v51, v83
	v_pk_mul_f32 v[12:13], v[14:15], v[16:17]
	v_pk_mul_f32 v[2:3], v[2:3], v[10:11]
	v_pk_mul_f32 v[10:11], v[4:5], v[12:13]
	v_pk_mul_f32 v[4:5], v[2:3], v[2:3]
	v_pk_mul_f32 v[14:15], v[48:49], v[76:77]
	v_pk_mul_f32 v[12:13], v[10:11], v[10:11]
	v_add_f32_e32 v4, v4, v5
	v_pk_mul_f32 v[6:7], v[6:7], v[14:15]
	v_add_f32_e32 v4, v12, v4
	v_pk_mul_f32 v[16:17], v[50:51], v[80:81]
	v_pk_mul_f32 v[14:15], v[6:7], v[6:7]
	v_add_f32_e32 v4, v13, v4
	v_pk_mul_f32 v[8:9], v[8:9], v[16:17]
	v_add_f32_e32 v4, v14, v4
	v_pk_mul_f32 v[16:17], v[8:9], v[8:9]
	v_add_f32_e32 v4, v15, v4
	v_add_f32_e32 v4, v16, v4
	v_add_f32_e32 v5, v17, v4
	ds_bpermute_b32 v14, v74, v5
	v_cvt_pk_bf16_f32 v4, v2, v3
	v_lshl_add_u64 v[12:13], v[46:47], 0, s[16:17]
	v_cvt_pk_bf16_f32 v6, v6, v7
	v_cvt_pk_bf16_f32 v7, v8, v9
	s_waitcnt lgkmcnt(0)
	v_add_f32_e32 v2, v5, v14
	ds_bpermute_b32 v3, v75, v2
	v_cvt_pk_bf16_f32 v5, v10, v11
	global_store_dwordx4 v[12:13], v[4:7], off offset:2048
	s_and_saveexec_b64 s[8:9], s[4:5]
	s_cbranch_execz .LBB0_1324
	s_waitcnt lgkmcnt(0)
	v_add_f32_e32 v2, v2, v3
	v_add_u32_e32 v3, v29, v64
	ds_write_b32 v3, v2 offset:8192
	s_branch .LBB0_1324

.LBB0_1858:
	ds_read_b128 v[152:155], v146
	ds_read_b128 v[156:159], v146 offset:1024
	ds_read_b128 v[160:163], v146 offset:2048
	ds_read_b128 v[164:167], v146 offset:3072
	s_add_u32 s36, s34, 0xfffc0080
	s_addc_u32 s37, s35, -1
	s_cmp_eq_u32 s63, 12
	s_cselect_b32 s37, s23, s37
	s_cselect_b32 s36, s61, s36
	s_cselect_b32 s65, s3, s62
	s_cselect_b32 s64, s38, s39
	v_lshl_add_u64 v[66:67], s[34:35], 0, v[136:137]
	s_add_i32 m0, s47, 0xc000
	ds_read_b128 v[168:171], v147
	ds_read_b128 v[172:175], v147 offset:1024
	ds_read_b128 v[176:179], v147 offset:2048
	ds_read_b128 v[180:183], v147 offset:3072
	ds_read_b128 v[184:187], v147 offset:4096
	ds_read_b128 v[188:191], v147 offset:5120
	ds_read_b128 v[192:195], v147 offset:6144
	ds_read_b128 v[196:199], v147 offset:7168
	global_load_lds_dwordx4 v[66:67], off
	v_lshl_add_u64 v[66:67], v[66:67], 0, s[4:5]
	s_add_i32 m0, s47, 0xe000
	s_nop 0
	global_load_lds_dwordx4 v[66:67], off
	s_waitcnt lgkmcnt(8)
	s_barrier
	s_waitcnt lgkmcnt(0)
	s_setprio 1
	s_waitcnt lgkmcnt(0)
	v_mfma_scale_f32_16x16x128_f8f6f4 v[126:129], v[152:159], v[168:175], v[126:129], v148, v148 op_sel_hi:[0,0,0]
	v_mfma_scale_f32_16x16x128_f8f6f4 v[118:121], v[160:167], v[168:175], v[118:121], v148, v148 op_sel_hi:[0,0,0]
	v_mfma_scale_f32_16x16x128_f8f6f4 v[110:113], v[152:159], v[176:183], v[110:113], v148, v148 op_sel_hi:[0,0,0]
	v_mfma_scale_f32_16x16x128_f8f6f4 v[102:105], v[160:167], v[176:183], v[102:105], v148, v148 op_sel_hi:[0,0,0]
	v_mfma_scale_f32_16x16x128_f8f6f4 v[140:143], v[152:159], v[184:191], v[94:97], v148, v148 op_sel_hi:[0,0,0]
	v_mfma_scale_f32_16x16x128_f8f6f4 v[216:219], v[160:167], v[184:191], v[86:89], v148, v148 op_sel_hi:[0,0,0]
	v_mfma_scale_f32_16x16x128_f8f6f4 v[220:223], v[152:159], v[192:199], v[78:81], v148, v148 op_sel_hi:[0,0,0]
	v_mfma_scale_f32_16x16x128_f8f6f4 v[224:227], v[160:167], v[192:199], v[208:211], v148, v148 op_sel_hi:[0,0,0]
	s_setprio 0
	s_barrier
	v_lshl_add_u64 v[138:139], s[64:65], 0, v[130:131]
	s_add_i32 s64, s57, s46
	s_mov_b32 m0, s64
	ds_read_b128 v[200:203], v149
	ds_read_b128 v[204:207], v149 offset:1024
	ds_read_b128 v[208:211], v149 offset:2048
	ds_read_b128 v[212:215], v149 offset:3072
	global_load_lds_dwordx4 v[138:139], off
	v_lshl_add_u64 v[66:67], v[138:139], 0, s[4:5]
	s_add_i32 m0, s64, 0x2000
	s_nop 0
	global_load_lds_dwordx4 v[66:67], off
	s_barrier
	s_waitcnt lgkmcnt(0)
	s_setprio 1
	s_waitcnt lgkmcnt(0)
	v_mfma_scale_f32_16x16x128_f8f6f4 v[122:125], v[200:207], v[168:175], v[122:125], v148, v148 op_sel_hi:[0,0,0]
	v_mfma_scale_f32_16x16x128_f8f6f4 v[114:117], v[208:215], v[168:175], v[114:117], v148, v148 op_sel_hi:[0,0,0]
	v_mfma_scale_f32_16x16x128_f8f6f4 v[106:109], v[200:207], v[176:183], v[106:109], v148, v148 op_sel_hi:[0,0,0]
	v_mfma_scale_f32_16x16x128_f8f6f4 v[98:101], v[208:215], v[176:183], v[98:101], v148, v148 op_sel_hi:[0,0,0]
	v_mfma_scale_f32_16x16x128_f8f6f4 v[176:179], v[200:207], v[184:191], v[90:93], v148, v148 op_sel_hi:[0,0,0]
	v_mfma_scale_f32_16x16x128_f8f6f4 v[180:183], v[208:215], v[184:191], v[82:85], v148, v148 op_sel_hi:[0,0,0]
	v_mfma_scale_f32_16x16x128_f8f6f4 v[184:187], v[200:207], v[192:199], v[74:77], v148, v148 op_sel_hi:[0,0,0]
	v_mfma_scale_f32_16x16x128_f8f6f4 v[188:191], v[208:215], v[192:199], v[10:13], v148, v148 op_sel_hi:[0,0,0]
	s_setprio 0
	s_mov_b32 m0, s47
	v_lshl_add_u64 v[144:145], s[36:37], 0, v[130:131]
	s_barrier
	ds_read_b128 v[66:69], v147 offset:16384
	ds_read_b128 v[70:73], v147 offset:17408
	ds_read_b128 v[74:77], v147 offset:18432
	ds_read_b128 v[78:81], v147 offset:19456
	ds_read_b128 v[82:85], v147 offset:20480
	ds_read_b128 v[86:89], v147 offset:21504
	ds_read_b128 v[90:93], v147 offset:22528
	ds_read_b128 v[94:97], v147 offset:23552
	global_load_lds_dwordx4 v[144:145], off
	v_lshl_add_u64 v[10:11], v[144:145], 0, s[4:5]
	s_mov_b32 m0, s48
	s_nop 0
	global_load_lds_dwordx4 v[10:11], off
	s_barrier
	s_waitcnt lgkmcnt(0)
	s_setprio 1
	s_waitcnt lgkmcnt(0)
	v_mfma_scale_f32_16x16x128_f8f6f4 v[62:65], v[152:159], v[66:73], v[62:65], v148, v148 op_sel_hi:[0,0,0]
	v_mfma_scale_f32_16x16x128_f8f6f4 v[54:57], v[160:167], v[66:73], v[54:57], v148, v148 op_sel_hi:[0,0,0]
	v_mfma_scale_f32_16x16x128_f8f6f4 v[46:49], v[152:159], v[74:81], v[46:49], v148, v148 op_sel_hi:[0,0,0]
	v_mfma_scale_f32_16x16x128_f8f6f4 v[244:247], v[160:167], v[90:97], v[244:247], v148, v148 op_sel_hi:[0,0,0]
	v_mfma_scale_f32_16x16x128_f8f6f4 v[228:231], v[160:167], v[74:81], v[38:41], v148, v148 op_sel_hi:[0,0,0]
	v_mfma_scale_f32_16x16x128_f8f6f4 v[232:235], v[152:159], v[82:89], v[30:33], v148, v148 op_sel_hi:[0,0,0]
	v_mfma_scale_f32_16x16x128_f8f6f4 v[236:239], v[160:167], v[82:89], v[22:25], v148, v148 op_sel_hi:[0,0,0]
	v_mfma_scale_f32_16x16x128_f8f6f4 v[240:243], v[152:159], v[90:97], v[14:17], v148, v148 op_sel_hi:[0,0,0]
	s_setprio 0
	s_barrier
	s_add_i32 s36, s58, s46
	v_lshl_add_u64 v[10:11], v[138:139], 0, s[6:7]
	s_mov_b32 m0, s36
	s_nop 0
	global_load_lds_dwordx4 v[10:11], off
	v_lshl_add_u64 v[10:11], v[138:139], 0, s[8:9]
	s_add_i32 m0, s36, 0x2000
	s_nop 0
	global_load_lds_dwordx4 v[10:11], off
	s_waitcnt vmcnt(6)
	s_barrier
	s_setprio 1
	v_mfma_scale_f32_16x16x128_f8f6f4 v[58:61], v[200:207], v[66:73], v[58:61], v148, v148 op_sel_hi:[0,0,0]
	v_mfma_scale_f32_16x16x128_f8f6f4 v[50:53], v[208:215], v[66:73], v[50:53], v148, v148 op_sel_hi:[0,0,0]
	v_mfma_scale_f32_16x16x128_f8f6f4 v[42:45], v[200:207], v[74:81], v[42:45], v148, v148 op_sel_hi:[0,0,0]
	v_mfma_scale_f32_16x16x128_f8f6f4 v[248:251], v[208:215], v[74:81], v[34:37], v148, v148 op_sel_hi:[0,0,0]
	v_mfma_scale_f32_16x16x128_f8f6f4 v[132:135], v[200:207], v[82:89], v[26:29], v148, v148 op_sel_hi:[0,0,0]
	v_mfma_scale_f32_16x16x128_f8f6f4 v[66:69], v[208:215], v[82:89], v[18:21], v148, v148 op_sel_hi:[0,0,0]
	v_mfma_scale_f32_16x16x128_f8f6f4 v[70:73], v[200:207], v[90:97], v[6:9], v148, v148 op_sel_hi:[0,0,0]
	v_mfma_scale_f32_16x16x128_f8f6f4 v[212:215], v[208:215], v[90:97], v[2:5], v148, v148 op_sel_hi:[0,0,0]
	s_setprio 0
	s_add_i32 s36, 0, 0x18000
	v_add_u32_e32 v10, s36, v1
	s_barrier
	s_nop 2
	ds_read_b128 v[2:5], v10
	ds_read_b128 v[6:9], v10 offset:1024
	ds_read_b128 v[152:155], v10 offset:2048
	ds_read_b128 v[156:159], v10 offset:3072
	s_mov_b32 m0, s49
	v_lshl_add_u64 v[74:75], v[144:145], 0, s[6:7]
	ds_read_b128 v[10:13], v147 offset:32768
	ds_read_b128 v[14:17], v147 offset:33792
	ds_read_b128 v[18:21], v147 offset:34816
	ds_read_b128 v[22:25], v147 offset:35840
	ds_read_b128 v[26:29], v147 offset:36864
	ds_read_b128 v[30:33], v147 offset:37888
	ds_read_b128 v[34:37], v147 offset:38912
	ds_read_b128 v[38:41], v147 offset:39936
	global_load_lds_dwordx4 v[74:75], off
	v_lshl_add_u64 v[74:75], v[144:145], 0, s[8:9]
	s_mov_b32 m0, s50
	s_nop 0
	global_load_lds_dwordx4 v[74:75], off
	s_waitcnt lgkmcnt(8)
	s_barrier
	s_waitcnt lgkmcnt(0)
	s_setprio 1
	s_waitcnt lgkmcnt(0)
	v_mfma_scale_f32_16x16x128_f8f6f4 v[126:129], v[2:9], v[10:17], v[126:129], v148, v148 op_sel_hi:[0,0,0]
	v_mfma_scale_f32_16x16x128_f8f6f4 v[118:121], v[152:159], v[10:17], v[118:121], v148, v148 op_sel_hi:[0,0,0]
	v_mfma_scale_f32_16x16x128_f8f6f4 v[110:113], v[2:9], v[18:25], v[110:113], v148, v148 op_sel_hi:[0,0,0]
	v_mfma_scale_f32_16x16x128_f8f6f4 v[102:105], v[152:159], v[18:25], v[102:105], v148, v148 op_sel_hi:[0,0,0]
	v_mfma_scale_f32_16x16x128_f8f6f4 v[94:97], v[2:9], v[26:33], v[140:143], v148, v148 op_sel_hi:[0,0,0]
	v_mfma_scale_f32_16x16x128_f8f6f4 v[86:89], v[152:159], v[26:33], v[216:219], v148, v148 op_sel_hi:[0,0,0]
	v_mfma_scale_f32_16x16x128_f8f6f4 v[78:81], v[2:9], v[34:41], v[220:223], v148, v148 op_sel_hi:[0,0,0]
	v_mfma_scale_f32_16x16x128_f8f6f4 v[208:211], v[152:159], v[34:41], v[224:227], v148, v148 op_sel_hi:[0,0,0]
	s_setprio 0
	s_barrier
	s_add_i32 s37, 0, 0x1c000
	v_add_u32_e32 v74, s37, v1
	s_add_i32 s36, s36, s46
	ds_read_b128 v[160:163], v74
	ds_read_b128 v[164:167], v74 offset:1024
	ds_read_b128 v[168:171], v74 offset:2048
	ds_read_b128 v[172:175], v74 offset:3072
	v_lshl_add_u64 v[74:75], v[138:139], 0, s[14:15]
	s_mov_b32 m0, s36
	s_nop 0
	global_load_lds_dwordx4 v[74:75], off
	v_lshl_add_u64 v[74:75], v[138:139], 0, s[16:17]
	s_add_i32 m0, s36, 0x2000
	s_nop 0
	global_load_lds_dwordx4 v[74:75], off
	s_barrier
	s_waitcnt lgkmcnt(0)
	s_setprio 1
	s_waitcnt lgkmcnt(0)
	v_mfma_scale_f32_16x16x128_f8f6f4 v[122:125], v[160:167], v[10:17], v[122:125], v148, v148 op_sel_hi:[0,0,0]
	v_mfma_scale_f32_16x16x128_f8f6f4 v[114:117], v[168:175], v[10:17], v[114:117], v148, v148 op_sel_hi:[0,0,0]
	v_mfma_scale_f32_16x16x128_f8f6f4 v[106:109], v[160:167], v[18:25], v[106:109], v148, v148 op_sel_hi:[0,0,0]
	v_mfma_scale_f32_16x16x128_f8f6f4 v[98:101], v[168:175], v[18:25], v[98:101], v148, v148 op_sel_hi:[0,0,0]
	v_mfma_scale_f32_16x16x128_f8f6f4 v[90:93], v[160:167], v[26:33], v[176:179], v148, v148 op_sel_hi:[0,0,0]
	v_mfma_scale_f32_16x16x128_f8f6f4 v[82:85], v[168:175], v[26:33], v[180:183], v148, v148 op_sel_hi:[0,0,0]
	v_mfma_scale_f32_16x16x128_f8f6f4 v[74:77], v[160:167], v[34:41], v[184:187], v148, v148 op_sel_hi:[0,0,0]
	v_mfma_scale_f32_16x16x128_f8f6f4 v[10:13], v[168:175], v[34:41], v[188:191], v148, v148 op_sel_hi:[0,0,0]
	s_setprio 0
	s_mov_b32 m0, s53
	v_lshl_add_u64 v[14:15], v[144:145], 0, s[14:15]
	s_barrier
	ds_read_b128 v[176:179], v147 offset:49152
	ds_read_b128 v[180:183], v147 offset:50176
	ds_read_b128 v[184:187], v147 offset:51200
	ds_read_b128 v[188:191], v147 offset:52224
	ds_read_b128 v[192:195], v147 offset:53248
	ds_read_b128 v[196:199], v147 offset:54272
	ds_read_b128 v[200:203], v147 offset:55296
	ds_read_b128 v[204:207], v147 offset:56320
	global_load_lds_dwordx4 v[14:15], off
	v_lshl_add_u64 v[14:15], v[144:145], 0, s[16:17]
	s_mov_b32 m0, s54
	s_nop 0
	global_load_lds_dwordx4 v[14:15], off
	s_barrier
	s_waitcnt lgkmcnt(0)
	s_setprio 1
	s_waitcnt lgkmcnt(0)
	v_mfma_scale_f32_16x16x128_f8f6f4 v[62:65], v[2:9], v[176:183], v[62:65], v148, v148 op_sel_hi:[0,0,0]
	v_mfma_scale_f32_16x16x128_f8f6f4 v[54:57], v[152:159], v[176:183], v[54:57], v148, v148 op_sel_hi:[0,0,0]
	v_mfma_scale_f32_16x16x128_f8f6f4 v[46:49], v[2:9], v[184:191], v[46:49], v148, v148 op_sel_hi:[0,0,0]
	v_mfma_scale_f32_16x16x128_f8f6f4 v[38:41], v[152:159], v[184:191], v[228:231], v148, v148 op_sel_hi:[0,0,0]
	v_mfma_scale_f32_16x16x128_f8f6f4 v[30:33], v[2:9], v[192:199], v[232:235], v148, v148 op_sel_hi:[0,0,0]
	v_mfma_scale_f32_16x16x128_f8f6f4 v[22:25], v[152:159], v[192:199], v[236:239], v148, v148 op_sel_hi:[0,0,0]
	v_mfma_scale_f32_16x16x128_f8f6f4 v[14:17], v[2:9], v[200:207], v[240:243], v148, v148 op_sel_hi:[0,0,0]
	v_mfma_scale_f32_16x16x128_f8f6f4 v[244:247], v[152:159], v[200:207], v[244:247], v148, v148 op_sel_hi:[0,0,0]
	s_setprio 0
	s_barrier
	s_add_i32 s36, s37, s46
	v_lshl_add_u64 v[2:3], v[138:139], 0, s[18:19]
	s_mov_b32 m0, s36
	s_nop 0
	global_load_lds_dwordx4 v[2:3], off
	v_lshl_add_u64 v[2:3], v[138:139], 0, s[20:21]
	s_add_i32 m0, s36, 0x2000
	s_nop 0
	global_load_lds_dwordx4 v[2:3], off
	s_waitcnt vmcnt(6)
	s_barrier
	s_setprio 1
	v_mfma_scale_f32_16x16x128_f8f6f4 v[58:61], v[160:167], v[176:183], v[58:61], v148, v148 op_sel_hi:[0,0,0]
	v_mfma_scale_f32_16x16x128_f8f6f4 v[50:53], v[168:175], v[176:183], v[50:53], v148, v148 op_sel_hi:[0,0,0]
	v_mfma_scale_f32_16x16x128_f8f6f4 v[42:45], v[160:167], v[184:191], v[42:45], v148, v148 op_sel_hi:[0,0,0]
	v_mfma_scale_f32_16x16x128_f8f6f4 v[34:37], v[168:175], v[184:191], v[248:251], v148, v148 op_sel_hi:[0,0,0]
	v_mfma_scale_f32_16x16x128_f8f6f4 v[26:29], v[160:167], v[192:199], v[132:135], v148, v148 op_sel_hi:[0,0,0]
	v_mfma_scale_f32_16x16x128_f8f6f4 v[18:21], v[168:175], v[192:199], v[66:69], v148, v148 op_sel_hi:[0,0,0]
	v_mfma_scale_f32_16x16x128_f8f6f4 v[6:9], v[160:167], v[200:207], v[70:73], v148, v148 op_sel_hi:[0,0,0]
	v_mfma_scale_f32_16x16x128_f8f6f4 v[2:5], v[168:175], v[200:207], v[212:215], v148, v148 op_sel_hi:[0,0,0]
	s_setprio 0
	s_add_i32 s63, s63, 2
	s_add_u32 s34, s34, 0x100
	s_addc_u32 s35, s35, 0
	s_add_u32 s39, s39, 0x100
	s_addc_u32 s62, s62, 0
	s_cmp_gt_u32 s63, 13
	s_barrier
	s_cbranch_scc0 .LBB0_1858
	v_mov_b32_e32 v68, v0
	s_cmp_gt_i32 s31, 7
	s_cselect_b64 vcc, -1, 0
	v_ashrrev_i32_e32 v69, 8, v68
	s_lshl_b32 s3, s30, 8
	v_bfe_u32 v71, v68, 2, 4
	v_lshl_add_u32 v66, v69, 6, s3
	v_and_b32_e32 v72, 3, v68
	v_or_b32_e32 v140, v66, v71
	v_bfe_u32 v70, v68, 6, 2
	v_lshlrev_b32_e32 v66, 2, v72
	v_ashrrev_i32_e32 v141, 31, v140
	v_lshl_or_b32 v73, v70, 5, v66
	v_lshlrev_b64 v[66:67], 10, v[140:141]
	v_lshl_add_u64 v[66:67], s[12:13], 0, v[66:67]
	v_lshlrev_b32_e32 v252, 2, v73
	v_lshl_add_u64 v[66:67], v[66:67], 0, v[252:253]
	global_load_dwordx4 v[152:155], v[66:67], off offset:512
	global_load_dwordx4 v[156:159], v[66:67], off
	global_load_dwordx4 v[160:163], v[66:67], off offset:576
	global_load_dwordx4 v[164:167], v[66:67], off offset:64
	v_lshl_or_b32 v69, v69, 2, v70
	v_and_b32_e32 v132, 15, v68
	v_mul_lo_u32 v69, v69, s59
	v_and_b32_e32 v68, 48, v68
	v_mul_u32_u24_e32 v70, 0x50, v132
	v_add_u32_e32 v69, s60, v69
	v_mul_u32_u24_e32 v71, 0x50, v71
	v_lshlrev_b32_e32 v72, 4, v72
	v_add3_u32 v141, v69, v70, v68
	v_add3_u32 v139, v69, v71, v72
	ds_write_b128 v141, v[126:129]
	ds_write_b128 v141, v[122:125] offset:1280
	ds_read_b128 v[122:125], v139
	ds_read_b128 v[126:129], v139 offset:1280
	s_lshl_b32 s30, s31, 8
	v_mov_b64_e32 v[142:143], s[10:11]
	s_ashr_i32 s31, s30, 31
	v_lshlrev_b32_e32 v144, 1, v73
	v_cndmask_b32_e32 v138, 1.0, v150, vcc
	s_lshl_b64 s[30:31], s[30:31], 1
	v_mad_i64_i32 v[68:69], s[34:35], v140, s52, v[142:143]
	v_mov_b32_e32 v145, v253
	v_lshl_add_u64 v[68:69], v[68:69], 0, s[30:31]
	v_lshl_add_u64 v[68:69], v[68:69], 0, v[144:145]
	s_waitcnt vmcnt(2) lgkmcnt(0)
	v_pk_mul_f32 v[70:71], v[128:129], v[154:155]
	v_pk_mul_f32 v[72:73], v[126:127], v[152:153]
	v_pk_mul_f32 v[132:133], v[124:125], v[154:155]
	v_pk_mul_f32 v[134:135], v[122:123], v[152:153]
	v_pk_fma_f32 v[70:71], v[124:125], v[158:159], v[70:71] neg_lo:[0,0,1] neg_hi:[0,0,1]
	v_pk_fma_f32 v[72:73], v[122:123], v[156:157], v[72:73] neg_lo:[0,0,1] neg_hi:[0,0,1]
	v_pk_fma_f32 v[122:123], v[128:129], v[158:159], v[132:133]
	v_pk_fma_f32 v[124:125], v[126:127], v[156:157], v[134:135]
	v_pk_mul_f32 v[70:71], v[138:139], v[70:71] op_sel_hi:[0,1]
	v_pk_mul_f32 v[72:73], v[138:139], v[72:73] op_sel_hi:[0,1]
	v_pk_mul_f32 v[122:123], v[138:139], v[122:123] op_sel_hi:[0,1]
	v_pk_mul_f32 v[124:125], v[138:139], v[124:125] op_sel_hi:[0,1]
	v_cvt_pk_bf16_f32 v72, v72, v73
	v_cvt_pk_bf16_f32 v73, v70, v71
	v_cvt_pk_bf16_f32 v70, v124, v125
	v_cvt_pk_bf16_f32 v71, v122, v123
	global_store_dwordx2 v[68:69], v[72:73], off
	global_store_dwordx2 v[68:69], v[70:71], off offset:256
	ds_write_b128 v141, v[118:121]
	ds_write_b128 v141, v[114:117] offset:1280
	ds_read_b128 v[114:117], v139 offset:1280
	ds_read_b128 v[118:121], v139
	s_waitcnt vmcnt(3) lgkmcnt(1)
	v_pk_mul_f32 v[66:67], v[116:117], v[162:163]
	v_pk_mul_f32 v[70:71], v[114:115], v[160:161]
	s_waitcnt lgkmcnt(0)
	v_pk_mul_f32 v[72:73], v[120:121], v[162:163]
	v_pk_mul_f32 v[122:123], v[118:119], v[160:161]
	s_waitcnt vmcnt(2)
	v_pk_fma_f32 v[66:67], v[120:121], v[166:167], v[66:67] neg_lo:[0, 0, 1] neg_hi:[0, 0, 1]
	v_pk_fma_f32 v[70:71], v[118:119], v[164:165], v[70:71] neg_lo:[0, 0, 1] neg_hi:[0, 0, 1]
	v_pk_fma_f32 v[72:73], v[116:117], v[166:167], v[72:73]
	v_pk_fma_f32 v[114:115], v[114:115], v[164:165], v[122:123]
	v_pk_mul_f32 v[66:67], v[138:139], v[66:67] op_sel_hi:[0, 1]
	v_pk_mul_f32 v[70:71], v[138:139], v[70:71] op_sel_hi:[0, 1]
	v_pk_mul_f32 v[72:73], v[138:139], v[72:73] op_sel_hi:[0, 1]
	v_pk_mul_f32 v[114:115], v[138:139], v[114:115] op_sel_hi:[0, 1]
	v_cvt_pk_bf16_f32 v70, v70, v71
	v_cvt_pk_bf16_f32 v71, v66, v67
	v_cvt_pk_bf16_f32 v66, v114, v115
	v_cvt_pk_bf16_f32 v67, v72, v73
	global_store_dwordx2 v[68:69], v[70:71], off offset:32
	global_store_dwordx2 v[68:69], v[66:67], off offset:288
	v_or_b32_e32 v66, 16, v140
	v_ashrrev_i32_e32 v67, 31, v66
	v_lshlrev_b64 v[68:69], 10, v[66:67]
	v_lshl_add_u64 v[68:69], s[12:13], 0, v[68:69]
	v_lshl_add_u64 v[68:69], v[68:69], 0, v[252:253]
	global_load_dwordx4 v[114:117], v[68:69], off offset:512
	global_load_dwordx4 v[118:121], v[68:69], off
	global_load_dwordx4 v[160:163], v[68:69], off offset:576
	global_load_dwordx4 v[164:167], v[68:69], off offset:64
	ds_write_b128 v141, v[110:113]
	ds_write_b128 v141, v[106:109] offset:1280
	ds_read_b128 v[106:109], v139
	ds_read_b128 v[110:113], v139 offset:1280
	v_mad_i64_i32 v[66:67], s[34:35], v66, s52, v[142:143]
	v_lshl_add_u64 v[66:67], v[66:67], 0, s[30:31]
	v_lshl_add_u64 v[66:67], v[66:67], 0, v[144:145]
	s_waitcnt vmcnt(3) lgkmcnt(0)
	v_pk_mul_f32 v[70:71], v[112:113], v[116:117]
	v_pk_mul_f32 v[72:73], v[110:111], v[114:115]
	v_pk_mul_f32 v[116:117], v[108:109], v[116:117]
	v_pk_mul_f32 v[114:115], v[106:107], v[114:115]
	s_waitcnt vmcnt(2)
	v_pk_fma_f32 v[70:71], v[108:109], v[120:121], v[70:71] neg_lo:[0,0,1] neg_hi:[0,0,1]
	v_pk_fma_f32 v[72:73], v[106:107], v[118:119], v[72:73] neg_lo:[0,0,1] neg_hi:[0,0,1]
	v_pk_fma_f32 v[106:107], v[112:113], v[120:121], v[116:117]
	v_pk_fma_f32 v[108:109], v[110:111], v[118:119], v[114:115]
	v_pk_mul_f32 v[70:71], v[138:139], v[70:71] op_sel_hi:[0,1]
	v_pk_mul_f32 v[72:73], v[138:139], v[72:73] op_sel_hi:[0,1]
	v_pk_mul_f32 v[106:107], v[138:139], v[106:107] op_sel_hi:[0,1]
	v_pk_mul_f32 v[108:109], v[138:139], v[108:109] op_sel_hi:[0,1]
	v_cvt_pk_bf16_f32 v72, v72, v73
	v_cvt_pk_bf16_f32 v73, v70, v71
	v_cvt_pk_bf16_f32 v70, v108, v109
	v_cvt_pk_bf16_f32 v71, v106, v107
	global_store_dwordx2 v[66:67], v[72:73], off
	global_store_dwordx2 v[66:67], v[70:71], off offset:256
	ds_write_b128 v141, v[102:105]
	ds_write_b128 v141, v[98:101] offset:1280
	ds_read_b128 v[98:101], v139 offset:1280
	ds_read_b128 v[102:105], v139
	s_waitcnt vmcnt(3) lgkmcnt(1)
	v_pk_mul_f32 v[68:69], v[100:101], v[162:163]
	v_pk_mul_f32 v[70:71], v[98:99], v[160:161]
	s_waitcnt lgkmcnt(0)
	v_pk_mul_f32 v[72:73], v[104:105], v[162:163]
	v_pk_mul_f32 v[106:107], v[102:103], v[160:161]
	s_waitcnt vmcnt(2)
	v_pk_fma_f32 v[68:69], v[104:105], v[166:167], v[68:69] neg_lo:[0, 0, 1] neg_hi:[0, 0, 1]
	v_pk_fma_f32 v[70:71], v[102:103], v[164:165], v[70:71] neg_lo:[0, 0, 1] neg_hi:[0, 0, 1]
	v_pk_fma_f32 v[72:73], v[100:101], v[166:167], v[72:73]
	v_pk_fma_f32 v[98:99], v[98:99], v[164:165], v[106:107]
	v_pk_mul_f32 v[68:69], v[138:139], v[68:69] op_sel_hi:[0, 1]
	v_pk_mul_f32 v[70:71], v[138:139], v[70:71] op_sel_hi:[0, 1]
	v_pk_mul_f32 v[72:73], v[138:139], v[72:73] op_sel_hi:[0, 1]
	v_pk_mul_f32 v[98:99], v[138:139], v[98:99] op_sel_hi:[0, 1]
	v_cvt_pk_bf16_f32 v70, v70, v71
	v_cvt_pk_bf16_f32 v71, v68, v69
	v_cvt_pk_bf16_f32 v68, v98, v99
	v_cvt_pk_bf16_f32 v69, v72, v73
	global_store_dwordx2 v[66:67], v[70:71], off offset:32
	global_store_dwordx2 v[66:67], v[68:69], off offset:288
	v_or_b32_e32 v66, 32, v140
	v_ashrrev_i32_e32 v67, 31, v66
	v_lshlrev_b64 v[68:69], 10, v[66:67]
	v_lshl_add_u64 v[68:69], s[12:13], 0, v[68:69]
	v_lshl_add_u64 v[68:69], v[68:69], 0, v[252:253]
	global_load_dwordx4 v[98:101], v[68:69], off offset:512
	global_load_dwordx4 v[102:105], v[68:69], off
	global_load_dwordx4 v[160:163], v[68:69], off offset:576
	global_load_dwordx4 v[164:167], v[68:69], off offset:64
	ds_write_b128 v141, v[94:97]
	ds_write_b128 v141, v[90:93] offset:1280
	ds_read_b128 v[90:93], v139
	ds_read_b128 v[94:97], v139 offset:1280
	v_mad_i64_i32 v[66:67], s[34:35], v66, s52, v[142:143]
	v_lshl_add_u64 v[66:67], v[66:67], 0, s[30:31]
	v_lshl_add_u64 v[66:67], v[66:67], 0, v[144:145]
	s_waitcnt vmcnt(3) lgkmcnt(0)
	v_pk_mul_f32 v[70:71], v[96:97], v[100:101]
	v_pk_mul_f32 v[72:73], v[94:95], v[98:99]
	v_pk_mul_f32 v[100:101], v[92:93], v[100:101]
	v_pk_mul_f32 v[98:99], v[90:91], v[98:99]
	s_waitcnt vmcnt(2)
	v_pk_fma_f32 v[70:71], v[92:93], v[104:105], v[70:71] neg_lo:[0,0,1] neg_hi:[0,0,1]
	v_pk_fma_f32 v[72:73], v[90:91], v[102:103], v[72:73] neg_lo:[0,0,1] neg_hi:[0,0,1]
	v_pk_fma_f32 v[90:91], v[96:97], v[104:105], v[100:101]
	v_pk_fma_f32 v[92:93], v[94:95], v[102:103], v[98:99]
	v_pk_mul_f32 v[70:71], v[138:139], v[70:71] op_sel_hi:[0,1]
	v_pk_mul_f32 v[72:73], v[138:139], v[72:73] op_sel_hi:[0,1]
	v_pk_mul_f32 v[90:91], v[138:139], v[90:91] op_sel_hi:[0,1]
	v_pk_mul_f32 v[92:93], v[138:139], v[92:93] op_sel_hi:[0,1]
	v_cvt_pk_bf16_f32 v72, v72, v73
	v_cvt_pk_bf16_f32 v73, v70, v71
	v_cvt_pk_bf16_f32 v70, v92, v93
	v_cvt_pk_bf16_f32 v71, v90, v91
	global_store_dwordx2 v[66:67], v[72:73], off
	global_store_dwordx2 v[66:67], v[70:71], off offset:256
	ds_write_b128 v141, v[86:89]
	ds_write_b128 v141, v[82:85] offset:1280
	ds_read_b128 v[82:85], v139 offset:1280
	ds_read_b128 v[86:89], v139
	s_waitcnt vmcnt(3) lgkmcnt(1)
	v_pk_mul_f32 v[68:69], v[84:85], v[162:163]
	v_pk_mul_f32 v[70:71], v[82:83], v[160:161]
	s_waitcnt lgkmcnt(0)
	v_pk_mul_f32 v[72:73], v[88:89], v[162:163]
	v_pk_mul_f32 v[90:91], v[86:87], v[160:161]
	s_waitcnt vmcnt(2)
	v_pk_fma_f32 v[68:69], v[88:89], v[166:167], v[68:69] neg_lo:[0, 0, 1] neg_hi:[0, 0, 1]
	v_pk_fma_f32 v[70:71], v[86:87], v[164:165], v[70:71] neg_lo:[0, 0, 1] neg_hi:[0, 0, 1]
	v_pk_fma_f32 v[72:73], v[84:85], v[166:167], v[72:73]
	v_pk_fma_f32 v[82:83], v[82:83], v[164:165], v[90:91]
	v_pk_mul_f32 v[68:69], v[138:139], v[68:69] op_sel_hi:[0, 1]
	v_pk_mul_f32 v[70:71], v[138:139], v[70:71] op_sel_hi:[0, 1]
	v_pk_mul_f32 v[72:73], v[138:139], v[72:73] op_sel_hi:[0, 1]
	v_pk_mul_f32 v[82:83], v[138:139], v[82:83] op_sel_hi:[0, 1]
	v_cvt_pk_bf16_f32 v70, v70, v71
	v_cvt_pk_bf16_f32 v71, v68, v69
	v_cvt_pk_bf16_f32 v68, v82, v83
	v_cvt_pk_bf16_f32 v69, v72, v73
	global_store_dwordx2 v[66:67], v[70:71], off offset:32
	global_store_dwordx2 v[66:67], v[68:69], off offset:288
	v_or_b32_e32 v66, 48, v140
	v_ashrrev_i32_e32 v67, 31, v66
	v_lshlrev_b64 v[68:69], 10, v[66:67]
	v_lshl_add_u64 v[68:69], s[12:13], 0, v[68:69]
	v_lshl_add_u64 v[68:69], v[68:69], 0, v[252:253]
	global_load_dwordx4 v[82:85], v[68:69], off offset:512
	global_load_dwordx4 v[86:89], v[68:69], off
	global_load_dwordx4 v[160:163], v[68:69], off offset:576
	global_load_dwordx4 v[164:167], v[68:69], off offset:64
	ds_write_b128 v141, v[78:81]
	ds_write_b128 v141, v[74:77] offset:1280
	ds_read_b128 v[74:77], v139
	ds_read_b128 v[78:81], v139 offset:1280
	v_mad_i64_i32 v[66:67], s[34:35], v66, s52, v[142:143]
	v_lshl_add_u64 v[66:67], v[66:67], 0, s[30:31]
	v_lshl_add_u64 v[90:91], v[66:67], 0, v[144:145]
	s_waitcnt vmcnt(3) lgkmcnt(0)
	v_pk_mul_f32 v[66:67], v[80:81], v[84:85]
	v_pk_mul_f32 v[70:71], v[78:79], v[82:83]
	v_pk_mul_f32 v[72:73], v[76:77], v[84:85]
	v_pk_mul_f32 v[82:83], v[74:75], v[82:83]
	s_waitcnt vmcnt(2)
	v_pk_fma_f32 v[66:67], v[76:77], v[88:89], v[66:67] neg_lo:[0,0,1] neg_hi:[0,0,1]
	v_pk_fma_f32 v[70:71], v[74:75], v[86:87], v[70:71] neg_lo:[0,0,1] neg_hi:[0,0,1]
	v_pk_fma_f32 v[72:73], v[80:81], v[88:89], v[72:73]
	v_pk_fma_f32 v[74:75], v[78:79], v[86:87], v[82:83]
	v_pk_mul_f32 v[66:67], v[138:139], v[66:67] op_sel_hi:[0,1]
	v_pk_mul_f32 v[70:71], v[138:139], v[70:71] op_sel_hi:[0,1]
	v_pk_mul_f32 v[72:73], v[138:139], v[72:73] op_sel_hi:[0,1]
	v_pk_mul_f32 v[74:75], v[138:139], v[74:75] op_sel_hi:[0,1]
	v_cvt_pk_bf16_f32 v70, v70, v71
	v_cvt_pk_bf16_f32 v71, v66, v67
	v_cvt_pk_bf16_f32 v66, v74, v75
	v_cvt_pk_bf16_f32 v67, v72, v73
	global_store_dwordx2 v[90:91], v[70:71], off
	global_store_dwordx2 v[90:91], v[66:67], off offset:256
	ds_write_b128 v141, v[208:211]
	ds_write_b128 v141, v[10:13] offset:1280
	ds_read_b128 v[66:69], v139 offset:1280
	ds_read_b128 v[70:73], v139
	s_waitcnt vmcnt(3) lgkmcnt(1)
	v_pk_mul_f32 v[10:11], v[68:69], v[162:163]
	v_pk_mul_f32 v[12:13], v[66:67], v[160:161]
	s_waitcnt lgkmcnt(0)
	v_pk_mul_f32 v[76:77], v[72:73], v[162:163]
	v_pk_mul_f32 v[74:75], v[70:71], v[160:161]
	s_waitcnt vmcnt(2)
	v_pk_fma_f32 v[10:11], v[72:73], v[166:167], v[10:11] neg_lo:[0, 0, 1] neg_hi:[0, 0, 1]
	v_pk_fma_f32 v[12:13], v[70:71], v[164:165], v[12:13] neg_lo:[0, 0, 1] neg_hi:[0, 0, 1]
	v_pk_fma_f32 v[68:69], v[68:69], v[166:167], v[76:77]
	v_pk_fma_f32 v[66:67], v[66:67], v[164:165], v[74:75]
	v_pk_mul_f32 v[10:11], v[138:139], v[10:11] op_sel_hi:[0, 1]
	v_pk_mul_f32 v[12:13], v[138:139], v[12:13] op_sel_hi:[0, 1]
	v_pk_mul_f32 v[68:69], v[138:139], v[68:69] op_sel_hi:[0, 1]
	v_pk_mul_f32 v[66:67], v[138:139], v[66:67] op_sel_hi:[0, 1]
	v_cvt_pk_bf16_f32 v12, v12, v13
	v_cvt_pk_bf16_f32 v13, v10, v11
	v_cvt_pk_bf16_f32 v10, v66, v67
	v_cvt_pk_bf16_f32 v11, v68, v69
	global_store_dwordx2 v[90:91], v[12:13], off offset:32
	global_store_dwordx2 v[90:91], v[10:11], off offset:288
	v_add_u32_e32 v10, 0x80, v140
	v_ashrrev_i32_e32 v11, 31, v10
	v_lshlrev_b64 v[12:13], 10, v[10:11]
	v_lshl_add_u64 v[12:13], s[12:13], 0, v[12:13]
	v_lshl_add_u64 v[12:13], v[12:13], 0, v[252:253]
	global_load_dwordx4 v[66:69], v[12:13], off offset:512
	global_load_dwordx4 v[70:73], v[12:13], off
	global_load_dwordx4 v[160:163], v[12:13], off offset:576
	global_load_dwordx4 v[164:167], v[12:13], off offset:64
	ds_write_b128 v141, v[62:65]
	ds_write_b128 v141, v[58:61] offset:1280
	ds_read_b128 v[58:61], v139
	ds_read_b128 v[62:65], v139 offset:1280
	v_mad_i64_i32 v[10:11], s[34:35], v10, s52, v[142:143]
	v_lshl_add_u64 v[10:11], v[10:11], 0, s[30:31]
	v_lshl_add_u64 v[10:11], v[10:11], 0, v[144:145]
	s_waitcnt vmcnt(3) lgkmcnt(0)
	v_pk_mul_f32 v[74:75], v[64:65], v[68:69]
	v_pk_mul_f32 v[76:77], v[62:63], v[66:67]
	v_pk_mul_f32 v[68:69], v[60:61], v[68:69]
	v_pk_mul_f32 v[66:67], v[58:59], v[66:67]
	s_waitcnt vmcnt(2)
	v_pk_fma_f32 v[60:61], v[60:61], v[72:73], v[74:75] neg_lo:[0,0,1] neg_hi:[0,0,1]
	v_pk_fma_f32 v[58:59], v[58:59], v[70:71], v[76:77] neg_lo:[0,0,1] neg_hi:[0,0,1]
	v_pk_fma_f32 v[64:65], v[64:65], v[72:73], v[68:69]
	v_pk_fma_f32 v[62:63], v[62:63], v[70:71], v[66:67]
	v_pk_mul_f32 v[60:61], v[138:139], v[60:61] op_sel_hi:[0,1]
	v_pk_mul_f32 v[58:59], v[138:139], v[58:59] op_sel_hi:[0,1]
	v_pk_mul_f32 v[64:65], v[138:139], v[64:65] op_sel_hi:[0,1]
	v_pk_mul_f32 v[62:63], v[138:139], v[62:63] op_sel_hi:[0,1]
	v_cvt_pk_bf16_f32 v58, v58, v59
	v_cvt_pk_bf16_f32 v59, v60, v61
	v_cvt_pk_bf16_f32 v60, v62, v63
	v_cvt_pk_bf16_f32 v61, v64, v65
	global_store_dwordx2 v[10:11], v[58:59], off
	global_store_dwordx2 v[10:11], v[60:61], off offset:256
	s_nop 0
	ds_write_b128 v141, v[54:57]
	ds_write_b128 v141, v[50:53] offset:1280
	ds_read_b128 v[50:53], v139 offset:1280
	ds_read_b128 v[54:57], v139
	s_waitcnt vmcnt(3) lgkmcnt(1)
	v_pk_mul_f32 v[12:13], v[52:53], v[162:163]
	v_pk_mul_f32 v[66:67], v[50:51], v[160:161]
	s_waitcnt lgkmcnt(0)
	v_pk_mul_f32 v[60:61], v[56:57], v[162:163]
	v_pk_mul_f32 v[58:59], v[54:55], v[160:161]
	s_waitcnt vmcnt(2)
	v_pk_fma_f32 v[12:13], v[56:57], v[166:167], v[12:13] neg_lo:[0, 0, 1] neg_hi:[0, 0, 1]
	v_pk_fma_f32 v[54:55], v[54:55], v[164:165], v[66:67] neg_lo:[0, 0, 1] neg_hi:[0, 0, 1]
	v_pk_fma_f32 v[52:53], v[52:53], v[166:167], v[60:61]
	v_pk_fma_f32 v[50:51], v[50:51], v[164:165], v[58:59]
	v_pk_mul_f32 v[12:13], v[138:139], v[12:13] op_sel_hi:[0, 1]
	v_pk_mul_f32 v[54:55], v[138:139], v[54:55] op_sel_hi:[0, 1]
	v_pk_mul_f32 v[52:53], v[138:139], v[52:53] op_sel_hi:[0, 1]
	v_pk_mul_f32 v[50:51], v[138:139], v[50:51] op_sel_hi:[0, 1]
	v_cvt_pk_bf16_f32 v54, v54, v55
	v_cvt_pk_bf16_f32 v55, v12, v13
	v_cvt_pk_bf16_f32 v12, v50, v51
	v_cvt_pk_bf16_f32 v13, v52, v53
	global_store_dwordx2 v[10:11], v[54:55], off offset:32
	global_store_dwordx2 v[10:11], v[12:13], off offset:288
	v_add_u32_e32 v10, 0x90, v140
	v_ashrrev_i32_e32 v11, 31, v10
	v_lshlrev_b64 v[12:13], 10, v[10:11]
	v_lshl_add_u64 v[12:13], s[12:13], 0, v[12:13]
	v_lshl_add_u64 v[12:13], v[12:13], 0, v[252:253]
	global_load_dwordx4 v[50:53], v[12:13], off offset:512
	global_load_dwordx4 v[54:57], v[12:13], off
	global_load_dwordx4 v[160:163], v[12:13], off offset:576
	global_load_dwordx4 v[164:167], v[12:13], off offset:64
	ds_write_b128 v141, v[46:49]
	ds_write_b128 v141, v[42:45] offset:1280
	ds_read_b128 v[42:45], v139
	ds_read_b128 v[46:49], v139 offset:1280
	v_mad_i64_i32 v[10:11], s[34:35], v10, s52, v[142:143]
	v_lshl_add_u64 v[10:11], v[10:11], 0, s[30:31]
	v_lshl_add_u64 v[10:11], v[10:11], 0, v[144:145]
	s_waitcnt vmcnt(3) lgkmcnt(0)
	v_pk_mul_f32 v[58:59], v[48:49], v[52:53]
	v_pk_mul_f32 v[60:61], v[46:47], v[50:51]
	v_pk_mul_f32 v[52:53], v[44:45], v[52:53]
	v_pk_mul_f32 v[50:51], v[42:43], v[50:51]
	s_waitcnt vmcnt(2)
	v_pk_fma_f32 v[44:45], v[44:45], v[56:57], v[58:59] neg_lo:[0,0,1] neg_hi:[0,0,1]
	v_pk_fma_f32 v[42:43], v[42:43], v[54:55], v[60:61] neg_lo:[0,0,1] neg_hi:[0,0,1]
	v_pk_fma_f32 v[48:49], v[48:49], v[56:57], v[52:53]
	v_pk_fma_f32 v[46:47], v[46:47], v[54:55], v[50:51]
	v_pk_mul_f32 v[44:45], v[138:139], v[44:45] op_sel_hi:[0,1]
	v_pk_mul_f32 v[42:43], v[138:139], v[42:43] op_sel_hi:[0,1]
	v_pk_mul_f32 v[48:49], v[138:139], v[48:49] op_sel_hi:[0,1]
	v_pk_mul_f32 v[46:47], v[138:139], v[46:47] op_sel_hi:[0,1]
	v_cvt_pk_bf16_f32 v42, v42, v43
	v_cvt_pk_bf16_f32 v43, v44, v45
	v_cvt_pk_bf16_f32 v44, v46, v47
	v_cvt_pk_bf16_f32 v45, v48, v49
	global_store_dwordx2 v[10:11], v[42:43], off
	global_store_dwordx2 v[10:11], v[44:45], off offset:256
	s_nop 0
	ds_write_b128 v141, v[38:41]
	ds_write_b128 v141, v[34:37] offset:1280
	ds_read_b128 v[34:37], v139 offset:1280
	ds_read_b128 v[38:41], v139
	s_waitcnt vmcnt(3) lgkmcnt(1)
	v_pk_mul_f32 v[12:13], v[36:37], v[162:163]
	v_pk_mul_f32 v[50:51], v[34:35], v[160:161]
	s_waitcnt lgkmcnt(0)
	v_pk_mul_f32 v[44:45], v[40:41], v[162:163]
	v_pk_mul_f32 v[42:43], v[38:39], v[160:161]
	s_waitcnt vmcnt(2)
	v_pk_fma_f32 v[12:13], v[40:41], v[166:167], v[12:13] neg_lo:[0, 0, 1] neg_hi:[0, 0, 1]
	v_pk_fma_f32 v[38:39], v[38:39], v[164:165], v[50:51] neg_lo:[0, 0, 1] neg_hi:[0, 0, 1]
	v_pk_fma_f32 v[36:37], v[36:37], v[166:167], v[44:45]
	v_pk_fma_f32 v[34:35], v[34:35], v[164:165], v[42:43]
	v_pk_mul_f32 v[12:13], v[138:139], v[12:13] op_sel_hi:[0, 1]
	v_pk_mul_f32 v[38:39], v[138:139], v[38:39] op_sel_hi:[0, 1]
	v_pk_mul_f32 v[36:37], v[138:139], v[36:37] op_sel_hi:[0, 1]
	v_pk_mul_f32 v[34:35], v[138:139], v[34:35] op_sel_hi:[0, 1]
	v_cvt_pk_bf16_f32 v38, v38, v39
	v_cvt_pk_bf16_f32 v39, v12, v13
	v_cvt_pk_bf16_f32 v12, v34, v35
	v_cvt_pk_bf16_f32 v13, v36, v37
	global_store_dwordx2 v[10:11], v[38:39], off offset:32
	global_store_dwordx2 v[10:11], v[12:13], off offset:288
	v_add_u32_e32 v10, 0xa0, v140
	v_ashrrev_i32_e32 v11, 31, v10
	v_lshlrev_b64 v[12:13], 10, v[10:11]
	v_lshl_add_u64 v[12:13], s[12:13], 0, v[12:13]
	v_lshl_add_u64 v[12:13], v[12:13], 0, v[252:253]
	global_load_dwordx4 v[34:37], v[12:13], off offset:512
	global_load_dwordx4 v[38:41], v[12:13], off
	global_load_dwordx4 v[160:163], v[12:13], off offset:576
	global_load_dwordx4 v[164:167], v[12:13], off offset:64
	ds_write_b128 v141, v[30:33]
	ds_write_b128 v141, v[26:29] offset:1280
	ds_read_b128 v[26:29], v139
	ds_read_b128 v[30:33], v139 offset:1280
	v_mad_i64_i32 v[10:11], s[34:35], v10, s52, v[142:143]
	v_lshl_add_u64 v[10:11], v[10:11], 0, s[30:31]
	v_lshl_add_u64 v[10:11], v[10:11], 0, v[144:145]
	s_waitcnt vmcnt(3) lgkmcnt(0)
	v_pk_mul_f32 v[42:43], v[32:33], v[36:37]
	v_pk_mul_f32 v[44:45], v[30:31], v[34:35]
	v_pk_mul_f32 v[36:37], v[28:29], v[36:37]
	v_pk_mul_f32 v[34:35], v[26:27], v[34:35]
	s_waitcnt vmcnt(2)
	v_pk_fma_f32 v[28:29], v[28:29], v[40:41], v[42:43] neg_lo:[0,0,1] neg_hi:[0,0,1]
	v_pk_fma_f32 v[26:27], v[26:27], v[38:39], v[44:45] neg_lo:[0,0,1] neg_hi:[0,0,1]
	v_pk_fma_f32 v[32:33], v[32:33], v[40:41], v[36:37]
	v_pk_fma_f32 v[30:31], v[30:31], v[38:39], v[34:35]
	v_pk_mul_f32 v[28:29], v[138:139], v[28:29] op_sel_hi:[0,1]
	v_pk_mul_f32 v[26:27], v[138:139], v[26:27] op_sel_hi:[0,1]
	v_pk_mul_f32 v[32:33], v[138:139], v[32:33] op_sel_hi:[0,1]
	v_pk_mul_f32 v[30:31], v[138:139], v[30:31] op_sel_hi:[0,1]
	v_cvt_pk_bf16_f32 v26, v26, v27
	v_cvt_pk_bf16_f32 v27, v28, v29
	v_cvt_pk_bf16_f32 v28, v30, v31
	v_cvt_pk_bf16_f32 v29, v32, v33
	global_store_dwordx2 v[10:11], v[26:27], off
	global_store_dwordx2 v[10:11], v[28:29], off offset:256
	s_nop 0
	ds_write_b128 v141, v[22:25]
	ds_write_b128 v141, v[18:21] offset:1280
	ds_read_b128 v[18:21], v139 offset:1280
	ds_read_b128 v[22:25], v139
	s_waitcnt vmcnt(3) lgkmcnt(1)
	v_pk_mul_f32 v[12:13], v[20:21], v[162:163]
	v_pk_mul_f32 v[34:35], v[18:19], v[160:161]
	s_waitcnt lgkmcnt(0)
	v_pk_mul_f32 v[28:29], v[24:25], v[162:163]
	v_pk_mul_f32 v[26:27], v[22:23], v[160:161]
	s_waitcnt vmcnt(2)
	v_pk_fma_f32 v[12:13], v[24:25], v[166:167], v[12:13] neg_lo:[0, 0, 1] neg_hi:[0, 0, 1]
	v_pk_fma_f32 v[22:23], v[22:23], v[164:165], v[34:35] neg_lo:[0, 0, 1] neg_hi:[0, 0, 1]
	v_pk_fma_f32 v[20:21], v[20:21], v[166:167], v[28:29]
	v_pk_fma_f32 v[18:19], v[18:19], v[164:165], v[26:27]
	v_pk_mul_f32 v[12:13], v[138:139], v[12:13] op_sel_hi:[0, 1]
	v_pk_mul_f32 v[22:23], v[138:139], v[22:23] op_sel_hi:[0, 1]
	v_pk_mul_f32 v[20:21], v[138:139], v[20:21] op_sel_hi:[0, 1]
	v_pk_mul_f32 v[18:19], v[138:139], v[18:19] op_sel_hi:[0, 1]
	v_cvt_pk_bf16_f32 v22, v22, v23
	v_cvt_pk_bf16_f32 v23, v12, v13
	v_cvt_pk_bf16_f32 v12, v18, v19
	v_cvt_pk_bf16_f32 v13, v20, v21
	global_store_dwordx2 v[10:11], v[22:23], off offset:32
	global_store_dwordx2 v[10:11], v[12:13], off offset:288
	v_add_u32_e32 v26, 0xb0, v140
	v_ashrrev_i32_e32 v27, 31, v26
	v_lshlrev_b64 v[10:11], 10, v[26:27]
	v_lshl_add_u64 v[10:11], s[12:13], 0, v[10:11]
	v_lshl_add_u64 v[28:29], v[10:11], 0, v[252:253]
	global_load_dwordx4 v[18:21], v[28:29], off offset:512
	global_load_dwordx4 v[22:25], v[28:29], off
	global_load_dwordx4 v[160:163], v[28:29], off offset:576
	global_load_dwordx4 v[164:167], v[28:29], off offset:64
	ds_write_b128 v141, v[14:17]
	ds_write_b128 v141, v[6:9] offset:1280
	ds_read_b128 v[10:13], v139
	ds_read_b128 v[14:17], v139 offset:1280
	v_mad_i64_i32 v[6:7], s[34:35], v26, s52, v[142:143]
	v_lshl_add_u64 v[6:7], v[6:7], 0, s[30:31]
	v_lshl_add_u64 v[26:27], v[6:7], 0, v[144:145]
	s_waitcnt vmcnt(3) lgkmcnt(0)
	v_pk_mul_f32 v[6:7], v[16:17], v[20:21]
	v_pk_mul_f32 v[8:9], v[14:15], v[18:19]
	v_pk_mul_f32 v[20:21], v[12:13], v[20:21]
	v_pk_mul_f32 v[18:19], v[10:11], v[18:19]
	s_waitcnt vmcnt(2)
	v_pk_fma_f32 v[6:7], v[12:13], v[24:25], v[6:7] neg_lo:[0,0,1] neg_hi:[0,0,1]
	v_pk_fma_f32 v[8:9], v[10:11], v[22:23], v[8:9] neg_lo:[0,0,1] neg_hi:[0,0,1]
	v_pk_fma_f32 v[10:11], v[16:17], v[24:25], v[20:21]
	v_pk_fma_f32 v[12:13], v[14:15], v[22:23], v[18:19]
	v_pk_mul_f32 v[6:7], v[138:139], v[6:7] op_sel_hi:[0,1]
	v_pk_mul_f32 v[8:9], v[138:139], v[8:9] op_sel_hi:[0,1]
	v_pk_mul_f32 v[10:11], v[138:139], v[10:11] op_sel_hi:[0,1]
	v_pk_mul_f32 v[12:13], v[138:139], v[12:13] op_sel_hi:[0,1]
	v_cvt_pk_bf16_f32 v8, v8, v9
	v_cvt_pk_bf16_f32 v9, v6, v7
	v_cvt_pk_bf16_f32 v6, v12, v13
	v_cvt_pk_bf16_f32 v7, v10, v11
	global_store_dwordx2 v[26:27], v[8:9], off
	global_store_dwordx2 v[26:27], v[6:7], off offset:256
	ds_write_b128 v141, v[244:247]
	ds_write_b128 v141, v[2:5] offset:1280
	ds_read_b128 v[2:5], v139 offset:1280
	ds_read_b128 v[6:9], v139
	s_waitcnt vmcnt(3) lgkmcnt(1)
	v_pk_mul_f32 v[18:19], v[4:5], v[162:163]
	v_pk_mul_f32 v[20:21], v[2:3], v[160:161]
	s_waitcnt lgkmcnt(0)
	v_pk_mul_f32 v[12:13], v[8:9], v[162:163]
	v_pk_mul_f32 v[10:11], v[6:7], v[160:161]
	s_waitcnt vmcnt(2)
	v_pk_fma_f32 v[8:9], v[8:9], v[166:167], v[18:19] neg_lo:[0, 0, 1] neg_hi:[0, 0, 1]
	v_pk_fma_f32 v[6:7], v[6:7], v[164:165], v[20:21] neg_lo:[0, 0, 1] neg_hi:[0, 0, 1]
	v_pk_fma_f32 v[4:5], v[4:5], v[166:167], v[12:13]
	v_pk_fma_f32 v[2:3], v[2:3], v[164:165], v[10:11]
	v_pk_mul_f32 v[8:9], v[138:139], v[8:9] op_sel_hi:[0, 1]
	v_pk_mul_f32 v[6:7], v[138:139], v[6:7] op_sel_hi:[0, 1]
	v_pk_mul_f32 v[4:5], v[138:139], v[4:5] op_sel_hi:[0, 1]
	v_pk_mul_f32 v[2:3], v[138:139], v[2:3] op_sel_hi:[0, 1]
	v_cvt_pk_bf16_f32 v6, v6, v7
	v_cvt_pk_bf16_f32 v7, v8, v9
	v_cvt_pk_bf16_f32 v2, v2, v3
	v_cvt_pk_bf16_f32 v3, v4, v5
	global_store_dwordx2 v[26:27], v[6:7], off offset:32
	global_store_dwordx2 v[26:27], v[2:3], off offset:288
	s_and_b64 vcc, exec, s[26:27]
	s_mov_b32 s31, s2
	s_mov_b32 s30, s22
	s_mov_b64 s[36:37], s[28:29]
	s_mov_b64 s[34:35], s[24:25]
	s_cbranch_vccz .LBB0_1850
	s_waitcnt vmcnt(0)
	s_cmpk_gt_u32 s33, 0xff
	s_cbranch_scc1 .LBB0_1862
	s_barrier
